# mixer-B loops unrolled x3: ring-slot offsets become immediates (no address VALU, no SGPR rotation)
# speedup vs baseline: 1.0005x; 1.0005x over previous
; __device__ __forceinline__ float softmax_rowmax(const f32x16& p0, const f32x16& p1) {
;   const float m0 = p1[0] + 0.0f; float a, b;
;   asm("v_max3_f32 %0, %1, %2, %3\n\tv_max3_f32 %0, %0, %4, %5\n\tv_max3_f32 %0, %0, %6, %7\n\tv_max3_f32 %0, %0, %8, %9\n\t"
;       "v_max3_f32 %0, %0, %10, %11\n\tv_max3_f32 %0, %0, %12, %13\n\tv_max3_f32 %0, %0, %14, %15\n\tv_max3_f32 %0, %0, %16, %17"
;       : "=&v"(a) : "v"(m0), "v"(p0[0]), "v"(p0[1]), "v"(p0[2]), "v"(p0[3]), "v"(p0[4]), "v"(p0[5]), "v"(p0[6]), "v"(p0[7]), "v"(p0[8]), "v"(p0[9]), "v"(p0[10]), "v"(p0[11]), "v"(p0[12]), "v"(p0[13]), "v"(p0[14]), "v"(p0[15]));
;   asm("v_max3_f32 %0, %1, %2, %3\n\tv_max3_f32 %0, %0, %4, %5\n\tv_max3_f32 %0, %0, %6, %7\n\tv_max3_f32 %0, %0, %8, %9\n\t"
;       "v_max3_f32 %0, %0, %10, %11\n\tv_max3_f32 %0, %0, %12, %13\n\tv_max3_f32 %0, %0, %14, %15\n\tv_max_f32 %0, %0, %16"
;       : "=&v"(b) : "v"(a), "v"(p1[1]), "v"(p1[2]), "v"(p1[3]), "v"(p1[4]), "v"(p1[5]), "v"(p1[6]), "v"(p1[7]), "v"(p1[8]), "v"(p1[9]), "v"(p1[10]), "v"(p1[11]), "v"(p1[12]), "v"(p1[13]), "v"(p1[14]), "v"(p1[15]));
;   return b;
; }
; __device__ __forceinline__ float softmax_shift(f32x16& p0, f32x16& p1, f32x16& negm, float pmax, bool first) {
;   asm volatile("s_nop 4" ::: "memory");
;   { auto rr = __builtin_amdgcn_permlane32_swap(__float_as_uint(pmax), __float_as_uint(pmax), false, false);
;     pmax = fmaxf(__uint_as_float(rr[0]), __uint_as_float(rr[1])); }
;   const float delta = first ? pmax : fmaxf(pmax, 0.f);
; #pragma unroll
;   for (int r = 0; r < 16; ++r) { p0[r] -= delta; p1[r] -= delta; negm[r] -= delta; }
;   return first ? 1.f : __builtin_amdgcn_exp2f(-delta);
; }
; __device__ __forceinline__ void softmax_exp_pack(f32x16& p0, f32x16& p1, bf16x8& pa0, bf16x8& pa1, bf16x8& pa2, bf16x8& pa3) {
; #pragma unroll
;   for (int r = 0; r < 16; ++r) { p0[r] = __builtin_amdgcn_exp2f(p0[r]); p1[r] = __builtin_amdgcn_exp2f(p1[r]); }
;     ...
;   ATT_PK4(p0, 0, pa0); ATT_PK4(p0, 8, pa1); ATT_PK4(p1, 0, pa2); ATT_PK4(p1, 8, pa3);
;     ...
; }
;     ...
;   for (int t = 0; t + 1 < NT; ++t) {
;     if constexpr (ABL & 1) { u32x4 w0 = {cvtpk(p0[0], p0[1]), cvtpk(p0[2], p0[3]), cvtpk(p0[4], p0[5]), cvtpk(p0[6], p0[7])}, w1 = {cvtpk(p0[8], p0[9]), cvtpk(p0[10], p0[11]), cvtpk(p0[12], p0[13]), cvtpk(p0[14], p0[15])};
.LBB0_281:
	v_mul_u32_u24_e32 v18, 0x90, v62
	v_add3_u32 v78, 0, v184, v18
	ds_read_b128 v[18:21], v78 offset:49152
	v_mad_u32_u24 v166, v62, s82, 0
	v_add_u32_e32 v172, v166, v184
	ds_read_b128 v[34:37], v172 offset:53760
	ds_read_b128 v[66:69], v78 offset:49184
	ds_read_b128 v[70:73], v78 offset:49216
	s_and_b32 s4, s92, 0x3fffffc0
	v_and_b32_e32 v63, 63, v63
	s_lshl_b32 s4, s4, 2
	s_add_i32 s6, s4, 0
	s_waitcnt lgkmcnt(3)
	v_mfma_f32_32x32x16_bf16 v[18:33], v[18:21], v[136:139], 0
	s_add_i32 s6, s6, 0x23080
	s_mov_b32 s97, 1
	s_waitcnt lgkmcnt(2)
	v_mfma_f32_32x32x16_bf16 v[34:49], v[34:37], v[136:139], 0
	s_waitcnt lgkmcnt(1)
	v_mfma_f32_32x32x16_bf16 v[18:33], v[66:69], v[140:143], v[18:33]
	ds_read_b128 v[66:69], v78 offset:53792
	ds_read_b128 v[74:77], v78 offset:49248
	s_waitcnt lgkmcnt(1)
	v_mfma_f32_32x32x16_bf16 v[34:49], v[66:69], v[140:143], v[34:49]
	v_mfma_f32_32x32x16_bf16 v[18:33], v[70:73], v[144:147], v[18:33]
	ds_read_b128 v[66:69], v78 offset:53824
	ds_read_b128 v[70:73], v78 offset:53856
	s_waitcnt lgkmcnt(1)
	v_mfma_f32_32x32x16_bf16 v[34:49], v[66:69], v[144:147], v[34:49]
	v_lshlrev_b32_e32 v67, 3, v63
	v_lshlrev_b32_e32 v69, 4, v63
	v_add_u32_e32 v66, 0xc000, v169
	v_and_b32_e32 v68, 24, v67
	v_and_b32_e32 v69, 0xc0, v69
	v_and_b32_e32 v67, 0x100, v67
	v_mfma_f32_32x32x16_bf16 v[18:33], v[74:77], v[148:151], v[18:33]
	v_lshlrev_b32_e32 v74, 1, v63
	v_and_b32_e32 v74, 32, v74
	s_waitcnt lgkmcnt(0)
	v_mfma_f32_32x32x16_bf16 v[34:49], v[70:73], v[148:151], v[34:49]
	s_barrier
	v_cmp_gt_u32_e64 s[4:5], 32, v63
	v_lshl_add_u32 v165, v62, 2, s6
	s_nop 9
	v_add_f32_e32 v62, 0, v34
	v_max3_f32 v63, v62, v18, v19
	v_max3_f32 v63, v63, v20, v21
	v_max3_f32 v63, v63, v22, v23
	v_max3_f32 v63, v63, v24, v25
	v_max3_f32 v63, v63, v26, v27
	v_max3_f32 v63, v63, v28, v29
	v_max3_f32 v63, v63, v30, v31
	v_max3_f32 v63, v63, v32, v33
	s_nop 4
	v_add3_u32 v68, 0, v68, v69
	v_max3_f32 v62, v63, v35, v36
	v_max3_f32 v62, v62, v37, v38
	v_max3_f32 v62, v62, v39, v40
	v_max3_f32 v62, v62, v41, v42
	v_max3_f32 v62, v62, v43, v44
	v_max3_f32 v62, v62, v45, v46
	v_max3_f32 v62, v62, v47, v48
	v_max_f32 v62, v62, v49
	v_add3_u32 v131, v68, v74, v67
	v_mov_b32_e32 v63, v62
	s_nop 1
	v_permlane32_swap_b32_e32 v62, v63
	v_max_f32_e32 v63, v63, v63
	v_max_f32_e32 v62, v62, v62
	v_max_f32_e32 v62, v62, v63
	v_sub_f32_e32 v18, v18, v62
	v_sub_f32_e32 v34, v34, v62
	v_sub_f32_e32 v19, v19, v62
	v_sub_f32_e32 v35, v35, v62
	v_sub_f32_e32 v20, v20, v62
	v_sub_f32_e32 v36, v36, v62
	v_sub_f32_e32 v21, v21, v62
	v_sub_f32_e32 v37, v37, v62
	v_sub_f32_e32 v22, v22, v62
	v_sub_f32_e32 v38, v38, v62
	v_sub_f32_e32 v23, v23, v62
	v_sub_f32_e32 v39, v39, v62
	v_sub_f32_e32 v24, v24, v62
	v_sub_f32_e32 v40, v40, v62
	v_sub_f32_e32 v25, v25, v62
	v_sub_f32_e32 v41, v41, v62
	v_sub_f32_e32 v26, v26, v62
	v_sub_f32_e32 v42, v42, v62
	v_sub_f32_e32 v27, v27, v62
	v_sub_f32_e32 v43, v43, v62
	v_sub_f32_e32 v28, v28, v62
	v_sub_f32_e32 v44, v44, v62
	v_sub_f32_e32 v29, v29, v62
	v_sub_f32_e32 v45, v45, v62
	v_sub_f32_e32 v30, v30, v62
	v_sub_f32_e32 v46, v46, v62
	v_sub_f32_e32 v31, v31, v62
	v_sub_f32_e32 v47, v47, v62
	v_sub_f32_e32 v32, v32, v62
	v_sub_f32_e32 v48, v48, v62
	v_sub_f32_e32 v33, v33, v62
	v_sub_f32_e32 v49, v49, v62
	v_exp_f32_e32 v18, v18
	v_exp_f32_e32 v34, v34
	v_exp_f32_e32 v19, v19
	v_exp_f32_e32 v35, v35
	v_exp_f32_e32 v20, v20
	v_exp_f32_e32 v36, v36
	v_exp_f32_e32 v21, v21
	v_exp_f32_e32 v37, v37
	v_exp_f32_e32 v22, v22
	v_exp_f32_e32 v38, v38
	v_exp_f32_e32 v23, v23
	v_exp_f32_e32 v39, v39
	v_exp_f32_e32 v24, v24
	v_exp_f32_e32 v40, v40
	v_exp_f32_e32 v25, v25
	v_exp_f32_e32 v41, v41
	v_exp_f32_e32 v26, v26
	v_exp_f32_e32 v42, v42
	v_exp_f32_e32 v27, v27
	v_exp_f32_e32 v43, v43
	v_exp_f32_e32 v28, v28
	v_exp_f32_e32 v44, v44
	v_exp_f32_e32 v29, v29
	v_exp_f32_e32 v45, v45
	v_exp_f32_e32 v30, v30
	v_exp_f32_e32 v46, v46
	v_exp_f32_e32 v31, v31
	v_exp_f32_e32 v47, v47
	v_exp_f32_e32 v32, v32
	v_exp_f32_e32 v48, v48
	v_exp_f32_e32 v33, v33
	v_exp_f32_e32 v49, v49
	v_sub_f32_e32 v82, 0, v62
	v_mov_b32_e32 v83, v82
	v_mov_b32_e32 v84, v82
	v_mov_b32_e32 v85, v82
	v_mov_b32_e32 v86, v82
	v_mov_b32_e32 v87, v82
	v_mov_b32_e32 v88, v82
	v_mov_b32_e32 v89, v82
	v_mov_b32_e32 v90, v82
	v_mov_b32_e32 v91, v82
	v_mov_b32_e32 v92, v82
	v_mov_b32_e32 v93, v82
	v_mov_b32_e32 v94, v82
	v_mov_b32_e32 v95, v82
	v_mov_b32_e32 v96, v82
	v_mov_b32_e32 v97, v82
	v_cvt_pk_bf16_f32 v98, v18, v19
	v_cvt_pk_bf16_f32 v99, v20, v21
	v_cvt_pk_bf16_f32 v100, v22, v23
	v_cvt_pk_bf16_f32 v101, v24, v25
	v_cvt_pk_bf16_f32 v102, v26, v27
	v_cvt_pk_bf16_f32 v103, v28, v29
	v_cvt_pk_bf16_f32 v104, v30, v31
	v_cvt_pk_bf16_f32 v105, v32, v33
	v_cvt_pk_bf16_f32 v106, v34, v35
	v_cvt_pk_bf16_f32 v107, v36, v37
	v_cvt_pk_bf16_f32 v108, v38, v39
	v_cvt_pk_bf16_f32 v109, v40, v41
	v_cvt_pk_bf16_f32 v110, v42, v43
	v_cvt_pk_bf16_f32 v111, v44, v45
	v_cvt_pk_bf16_f32 v112, v46, v47
	v_cvt_pk_bf16_f32 v113, v48, v49
	s_waitcnt vmcnt(1)
	ds_write_b128 v66, v[58:61] offset:18432
	ds_write_b128 v64, v[50:53] offset:16384
	s_waitcnt vmcnt(0)
	ds_write_b128 v65, v[54:57] offset:16384
	ds_read_b64_tr_b16 v[18:19], v131
	ds_read_b64_tr_b16 v[20:21], v131 offset:2048
	ds_read_b64_tr_b16 v[34:35], v131 offset:4096
	ds_read_b64_tr_b16 v[36:37], v131 offset:6144
	ds_read_b64_tr_b16 v[38:39], v131 offset:8192
	ds_read_b64_tr_b16 v[40:41], v131 offset:10240
	ds_read_b64_tr_b16 v[42:43], v131 offset:12288
	ds_read_b64_tr_b16 v[44:45], v131 offset:14336
	s_waitcnt lgkmcnt(8)
	s_barrier
; #define ATT_SBAR() __builtin_amdgcn_sched_barrier(0)
; __device__ __forceinline__ float softmax_rowmax(const f32x16& p0, const f32x16& p1) {
;   const float m0 = p1[0] + 0.0f; float a, b;
;   asm("v_max3_f32 %0, %1, %2, %3\n\tv_max3_f32 %0, %0, %4, %5\n\tv_max3_f32 %0, %0, %6, %7\n\tv_max3_f32 %0, %0, %8, %9\n\t"
;       "v_max3_f32 %0, %0, %10, %11\n\tv_max3_f32 %0, %0, %12, %13\n\tv_max3_f32 %0, %0, %14, %15\n\tv_max3_f32 %0, %0, %16, %17"
;       : "=&v"(a) : "v"(m0), "v"(p0[0]), "v"(p0[1]), "v"(p0[2]), "v"(p0[3]), "v"(p0[4]), "v"(p0[5]), "v"(p0[6]), "v"(p0[7]), "v"(p0[8]), "v"(p0[9]), "v"(p0[10]), "v"(p0[11]), "v"(p0[12]), "v"(p0[13]), "v"(p0[14]), "v"(p0[15]));
;   asm("v_max3_f32 %0, %1, %2, %3\n\tv_max3_f32 %0, %0, %4, %5\n\tv_max3_f32 %0, %0, %6, %7\n\tv_max3_f32 %0, %0, %8, %9\n\t"
;       "v_max3_f32 %0, %0, %10, %11\n\tv_max3_f32 %0, %0, %12, %13\n\tv_max3_f32 %0, %0, %14, %15\n\tv_max_f32 %0, %0, %16"
;       : "=&v"(b) : "v"(a), "v"(p1[1]), "v"(p1[2]), "v"(p1[3]), "v"(p1[4]), "v"(p1[5]), "v"(p1[6]), "v"(p1[7]), "v"(p1[8]), "v"(p1[9]), "v"(p1[10]), "v"(p1[11]), "v"(p1[12]), "v"(p1[13]), "v"(p1[14]), "v"(p1[15]));
;   return b;
;     ...
;   for (int t = 0; t + 1 < NT; ++t) {
;     if constexpr (ABL & 1) { u32x4 w0 = {cvtpk(p0[0], p0[1]), cvtpk(p0[2], p0[3]), cvtpk(p0[4], p0[5]), cvtpk(p0[6], p0[7])}, w1 = {cvtpk(p0[8], p0[9]), cvtpk(p0[10], p0[11]), cvtpk(p0[12], p0[13]), cvtpk(p0[14], p0[15])};
;         u32x4 w2 = {cvtpk(p1[0], p1[1]), cvtpk(p1[2], p1[3]), cvtpk(p1[4], p1[5]), cvtpk(p1[6], p1[7])}, w3 = {cvtpk(p1[8], p1[9]), cvtpk(p1[10], p1[11]), cvtpk(p1[12], p1[13]), cvtpk(p1[14], p1[15])};
;         pa0 = *reinterpret_cast<bf16x8*>(&w0); pa1 = *reinterpret_cast<bf16x8*>(&w1); pa2 = *reinterpret_cast<bf16x8*>(&w2); pa3 = *reinterpret_cast<bf16x8*>(&w3); }
;     else { ATT_SOFTMAX(t == 0); }
;     if constexpr (!(ABL & 4)) { ATT_WRITE_K(k2); ATT_WRITE_V(v1); }
;     ATT_SBAR();
; #pragma unroll
;     for (int ks = 0; ks < 4; ++ks) ATT_VPAIR(va, v0, 0, ks);
;     asm volatile("s_waitcnt lgkmcnt(8)" ::: "memory"); ATT_BAR();
;     ATT_XSECTION(true);
;     if constexpr (!(ABL & 4)) { const int tk = (t + 3 < NT) ? t + 3 : NT - 1, tv = (t + 2 < NT) ? t + 2 : NT - 1; ATT_LOAD_K(tk); ATT_LOAD_V(tv); }
;     ATT_BAR();
;     { const int tk_ = k0; k0 = k1; k1 = k2; k2 = tk_; const int tv_ = v0; v0 = v1; v1 = v2; v2 = tv_; }
;   }
	s_setprio 2
	s_waitcnt lgkmcnt(6)
	v_mfma_f32_32x32x16_bf16 v[18:33], v[98:101], v[18:21], 0
	ds_read_b64_tr_b16 v[46:47], v131 offset:512
	ds_read_b64_tr_b16 v[48:49], v131 offset:2560
	s_waitcnt lgkmcnt(6)
	v_mfma_f32_32x32x16_bf16 v[18:33], v[102:105], v[34:37], v[18:33]
	ds_read_b64_tr_b16 v[50:51], v131 offset:4608
	ds_read_b64_tr_b16 v[52:53], v131 offset:6656
	s_waitcnt lgkmcnt(6)
	v_mfma_f32_32x32x16_bf16 v[18:33], v[106:109], v[38:41], v[18:33]
	ds_read_b64_tr_b16 v[54:55], v131 offset:8704
	ds_read_b64_tr_b16 v[56:57], v131 offset:10752
	s_waitcnt lgkmcnt(6)
	v_mfma_f32_32x32x16_bf16 v[18:33], v[110:113], v[42:45], v[18:33]
	ds_read_b64_tr_b16 v[58:59], v131 offset:12800
	ds_read_b64_tr_b16 v[60:61], v131 offset:14848
	s_waitcnt lgkmcnt(6)
	v_mfma_f32_32x32x16_bf16 v[34:49], v[98:101], v[46:49], 0
	ds_read_b64_tr_b16 v[62:63], v131 offset:1024
	ds_read_b64_tr_b16 v[64:65], v131 offset:3072
	s_waitcnt lgkmcnt(6)
	v_mfma_f32_32x32x16_bf16 v[34:49], v[102:105], v[50:53], v[34:49]
	ds_read_b64_tr_b16 v[66:67], v131 offset:5120
	ds_read_b64_tr_b16 v[68:69], v131 offset:7168
	s_waitcnt lgkmcnt(6)
	v_mfma_f32_32x32x16_bf16 v[34:49], v[106:109], v[54:57], v[34:49]
	ds_read_b64_tr_b16 v[70:71], v131 offset:9216
	ds_read_b64_tr_b16 v[72:73], v131 offset:11264
	s_waitcnt lgkmcnt(6)
	v_mfma_f32_32x32x16_bf16 v[34:49], v[110:113], v[58:61], v[34:49]
	ds_read_b64_tr_b16 v[74:75], v131 offset:13312
	ds_read_b64_tr_b16 v[76:77], v131 offset:15360
	s_waitcnt lgkmcnt(6)
	v_mfma_f32_32x32x16_bf16 v[50:65], v[98:101], v[62:65], 0
	ds_read_b64_tr_b16 v[78:79], v131 offset:1536
	ds_read_b64_tr_b16 v[80:81], v131 offset:3584
	s_waitcnt lgkmcnt(6)
	v_mfma_f32_32x32x16_bf16 v[50:65], v[102:105], v[66:69], v[50:65]
	ds_read_b64_tr_b16 v[114:115], v131 offset:5632
	ds_read_b64_tr_b16 v[116:117], v131 offset:7680
	s_waitcnt lgkmcnt(6)
	v_mfma_f32_32x32x16_bf16 v[50:65], v[106:109], v[70:73], v[50:65]
	ds_read_b64_tr_b16 v[118:119], v131 offset:9728
	ds_read_b64_tr_b16 v[120:121], v131 offset:11776
	s_waitcnt lgkmcnt(6)
	v_mfma_f32_32x32x16_bf16 v[50:65], v[110:113], v[74:77], v[50:65]
	ds_read_b64_tr_b16 v[122:123], v131 offset:13824
	ds_read_b64_tr_b16 v[124:125], v131 offset:15872
	s_waitcnt lgkmcnt(6)
	v_mfma_f32_32x32x16_bf16 v[66:81], v[98:101], v[78:81], 0
	ds_read_b128 v[126:129], v172 offset:58368
	s_waitcnt lgkmcnt(5)
	v_mfma_f32_32x32x16_bf16 v[66:81], v[102:105], v[114:117], v[66:81]
	ds_read_b128 v[152:155], v172 offset:62976
	s_waitcnt lgkmcnt(4)
	v_mfma_f32_32x32x16_bf16 v[66:81], v[106:109], v[118:121], v[66:81]
	ds_read_b128 v[156:159], v172 offset:58400
	s_waitcnt lgkmcnt(3)
	v_mfma_f32_32x32x16_bf16 v[66:81], v[110:113], v[122:125], v[66:81]
	ds_read_b128 v[160:163], v172 offset:63008
	v_mfma_f32_4x4x4_16b_bf16 v[240:243], v[98:99], v[132:133], 0
	ds_read_b128 v[174:177], v172 offset:58432
	v_mfma_f32_4x4x4_16b_bf16 v[244:247], v[100:101], v[132:133], 0
	v_mfma_f32_4x4x4_16b_bf16 v[240:243], v[102:103], v[132:133], v[240:243]
	ds_read_b128 v[178:181], v172 offset:63040
	v_mfma_f32_4x4x4_16b_bf16 v[244:247], v[104:105], v[132:133], v[244:247]
	v_mfma_f32_4x4x4_16b_bf16 v[240:243], v[106:107], v[132:133], v[240:243]
	ds_read_b128 v[186:189], v172 offset:58464
	v_mfma_f32_4x4x4_16b_bf16 v[244:247], v[108:109], v[132:133], v[244:247]
	v_mfma_f32_4x4x4_16b_bf16 v[240:243], v[110:111], v[132:133], v[240:243]
	ds_read_b128 v[190:193], v172 offset:63072
	v_mfma_f32_4x4x4_16b_bf16 v[244:247], v[112:113], v[132:133], v[244:247]
	s_waitcnt lgkmcnt(7)
	v_mfma_f32_32x32x16_bf16 v[98:113], v[126:129], v[136:139], v[82:97]
	v_mov_b64_e32 v[128:129], v[96:97]
	v_mov_b64_e32 v[126:127], v[94:95]
	v_mov_b64_e32 v[124:125], v[92:93]
	v_mov_b64_e32 v[122:123], v[90:91]
	v_mov_b64_e32 v[120:121], v[88:89]
	v_mov_b64_e32 v[118:119], v[86:87]
	v_mov_b64_e32 v[116:117], v[84:85]
	v_mov_b64_e32 v[114:115], v[82:83]
	s_waitcnt lgkmcnt(6)
	s_nop 0
	v_mfma_f32_32x32x16_bf16 v[114:129], v[152:155], v[136:139], v[114:129]
	s_waitcnt lgkmcnt(5)
	v_mfma_f32_32x32x16_bf16 v[98:113], v[156:159], v[140:143], v[98:113]
	s_waitcnt lgkmcnt(4)
	v_mfma_f32_32x32x16_bf16 v[114:129], v[160:163], v[140:143], v[114:129]
	s_waitcnt lgkmcnt(3)
	v_mfma_f32_32x32x16_bf16 v[98:113], v[174:177], v[144:147], v[98:113]
	s_waitcnt lgkmcnt(2)
	v_mfma_f32_32x32x16_bf16 v[114:129], v[178:181], v[144:147], v[114:129]
	s_waitcnt lgkmcnt(1)
	v_mfma_f32_32x32x16_bf16 v[98:113], v[186:189], v[148:151], v[98:113]
	s_waitcnt lgkmcnt(0)
	v_mfma_f32_32x32x16_bf16 v[114:129], v[190:193], v[148:151], v[114:129]
	s_setprio 0
	s_mov_b32 s14, s10
	s_mov_b32 s15, s11
	buffer_load_dwordx4 v[224:227], v170, s[8:11], s85 offen
	buffer_load_dwordx4 v[228:231], v171, s[12:15], s83 offen
	buffer_load_dwordx4 v[232:235], v171, s[12:15], s86 offen
	s_barrier
	s_mov_b32 s95, 0x8000
	s_movk_i32 s15, 0x4000
	s_movk_i32 s18, 0x2400
	s_mov_b32 s94, 0
	s_movk_i32 s14, 0x4800
	s_mov_b32 s36, 0x70000
	s_mov_b32 s93, 0
	v_add_f32_e32 v173, 0, v114
	v_max3_f32 v174, v173, v98, v99
	v_max3_f32 v174, v174, v100, v101
	v_max3_f32 v174, v174, v102, v103
	v_max3_f32 v174, v174, v104, v105
	v_max3_f32 v174, v174, v106, v107
	v_max3_f32 v174, v174, v108, v109
	v_max3_f32 v174, v174, v110, v111
	v_max3_f32 v174, v174, v112, v113
	v_max3_f32 v173, v174, v115, v116
	v_max3_f32 v173, v173, v117, v118
	v_max3_f32 v173, v173, v119, v120
	v_max3_f32 v173, v173, v121, v122
	v_max3_f32 v173, v173, v123, v124
	v_max3_f32 v173, v173, v125, v126
	v_max3_f32 v173, v173, v127, v128
	v_max_f32 v173, v173, v129
	v_add_u32_e32 v248, 0x8000, v169
	v_add_u32_e32 v249, 0x8000, v172
.LBB0_282:
.Lu3_b1_0:
	v_cmp_ge_f32_e32 vcc, s60, v173
	s_cmp_eq_u64 vcc, exec
	s_cbranch_scc0 .Lu3_rare_b1_0
; #define ATT_SBAR() __builtin_amdgcn_sched_barrier(0)
; #define ATT_PK4(P, BASE, OUT) do { u32x4 w = {cvtpk(P[BASE + 0], P[BASE + 1]), cvtpk(P[BASE + 2], P[BASE + 3]), cvtpk(P[BASE + 4], P[BASE + 5]), cvtpk(P[BASE + 6], P[BASE + 7])}; \
;     OUT = *reinterpret_cast<bf16x8*>(&w); } while (0)
; #define ATT_WRITE_K(so) do { *(bf16x8*)(K_lds + (so) + kswz<DQK>(kr, kc * 2)) = sk0; if constexpr (DQK == 128) *(bf16x8*)(K_lds + (so) + kswz<DQK>(32 + kr, kc * 2)) = sk1; } while (0)
; #define ATT_WRITE_V(so) do { *(bf16x8*)(V_lds + (so) + vst0) = sv0; *(bf16x8*)(V_lds + (so) + vst1) = sv1; } while (0)
; #define ATT_BAR() do { ATT_SBAR(); asm volatile("s_barrier" ::: "memory"); ATT_SBAR(); } while (0)
; #define ATT_VPAIR(buf, so, blk, ks) do { if constexpr (!(ABL & 8) && !(ABL & 32)) { buf[2 * (ks)] = vtr(vq0 + (so) + v_rd_off(blk, ks, 0)); buf[2 * (ks) + 1] = vtr(vq0 + (so) + v_rd_off(blk, ks, 1)); } } while (0)
; __device__ __forceinline__ void softmax_exp_pack(f32x16& p0, f32x16& p1, bf16x8& pa0, bf16x8& pa1, bf16x8& pa2, bf16x8& pa3) {
; #pragma unroll
;   for (int r = 0; r < 16; ++r) { p0[r] = __builtin_amdgcn_exp2f(p0[r]); p1[r] = __builtin_amdgcn_exp2f(p1[r]); }
;     ...
;   ATT_PK4(p0, 0, pa0); ATT_PK4(p0, 8, pa1); ATT_PK4(p1, 0, pa2); ATT_PK4(p1, 8, pa3);
;     ...
;     if constexpr (!(ABL & 4)) { ATT_WRITE_K(k2); ATT_WRITE_V(v1); }
;     ATT_SBAR();
; #pragma unroll
;     for (int ks = 0; ks < 4; ++ks) ATT_VPAIR(va, v0, 0, ks);
;     asm volatile("s_waitcnt lgkmcnt(8)" ::: "memory"); ATT_BAR();
.LBB0_283:
	v_exp_f32_e32 v98, v98
	v_exp_f32_e32 v114, v114
	v_exp_f32_e32 v99, v99
	v_exp_f32_e32 v115, v115
	v_exp_f32_e32 v100, v100
	v_exp_f32_e32 v101, v101
	v_exp_f32_e32 v102, v102
	v_exp_f32_e32 v103, v103
	v_exp_f32_e32 v106, v106
	v_exp_f32_e32 v107, v107
	v_exp_f32_e32 v116, v116
	v_exp_f32_e32 v117, v117
	v_exp_f32_e32 v118, v118
	v_exp_f32_e32 v119, v119
	v_exp_f32_e32 v104, v104
	v_exp_f32_e32 v120, v120
	v_exp_f32_e32 v105, v105
	v_exp_f32_e32 v121, v121
	v_exp_f32_e32 v122, v122
	v_exp_f32_e32 v123, v123
	v_exp_f32_e32 v108, v108
	v_exp_f32_e32 v124, v124
	v_exp_f32_e32 v109, v109
	v_exp_f32_e32 v125, v125
	v_exp_f32_e32 v110, v110
	v_exp_f32_e32 v126, v126
	v_exp_f32_e32 v111, v111
	v_exp_f32_e32 v127, v127
	v_exp_f32_e32 v112, v112
	v_exp_f32_e32 v128, v128
	v_exp_f32_e32 v113, v113
	v_exp_f32_e32 v129, v129
	v_cvt_pk_bf16_f32 v2, v98, v99
	v_cvt_pk_bf16_f32 v3, v100, v101
	v_cvt_pk_bf16_f32 v4, v102, v103
	v_cvt_pk_bf16_f32 v6, v106, v107
	v_cvt_pk_bf16_f32 v10, v114, v115
	v_cvt_pk_bf16_f32 v5, v104, v105
	v_cvt_pk_bf16_f32 v7, v108, v109
	v_cvt_pk_bf16_f32 v8, v110, v111
	v_cvt_pk_bf16_f32 v9, v112, v113
	v_cvt_pk_bf16_f32 v11, v116, v117
	v_cvt_pk_bf16_f32 v12, v118, v119
	v_cvt_pk_bf16_f32 v13, v120, v121
	v_cvt_pk_bf16_f32 v14, v122, v123
	v_cvt_pk_bf16_f32 v15, v124, v125
	v_cvt_pk_bf16_f32 v16, v126, v127
	v_cvt_pk_bf16_f32 v17, v128, v129
	s_waitcnt vmcnt(0)
	ds_write_b128 v248, v[224:227] offset:16384
	ds_write_b128 v167, v[228:231] offset:32768
	ds_write_b128 v168, v[232:235] offset:32768
	ds_read_b128 v[152:155], v249 offset:34816
	ds_read_b128 v[156:159], v249 offset:39424
	ds_read_b128 v[160:163], v249 offset:34848
	ds_read_b128 v[176:179], v249 offset:39456
	s_waitcnt lgkmcnt(4)
	s_barrier
; #define ATT_SBAR() __builtin_amdgcn_sched_barrier(0)
; __device__ __forceinline__ float softmax_rowmax(const f32x16& p0, const f32x16& p1) {
;   const float m0 = p1[0] + 0.0f; float a, b;
;   asm("v_max3_f32 %0, %1, %2, %3\n\tv_max3_f32 %0, %0, %4, %5\n\tv_max3_f32 %0, %0, %6, %7\n\tv_max3_f32 %0, %0, %8, %9\n\t"
;       "v_max3_f32 %0, %0, %10, %11\n\tv_max3_f32 %0, %0, %12, %13\n\tv_max3_f32 %0, %0, %14, %15\n\tv_max3_f32 %0, %0, %16, %17"
;       : "=&v"(a) : "v"(m0), "v"(p0[0]), "v"(p0[1]), "v"(p0[2]), "v"(p0[3]), "v"(p0[4]), "v"(p0[5]), "v"(p0[6]), "v"(p0[7]), "v"(p0[8]), "v"(p0[9]), "v"(p0[10]), "v"(p0[11]), "v"(p0[12]), "v"(p0[13]), "v"(p0[14]), "v"(p0[15]));
;   asm("v_max3_f32 %0, %1, %2, %3\n\tv_max3_f32 %0, %0, %4, %5\n\tv_max3_f32 %0, %0, %6, %7\n\tv_max3_f32 %0, %0, %8, %9\n\t"
;       "v_max3_f32 %0, %0, %10, %11\n\tv_max3_f32 %0, %0, %12, %13\n\tv_max3_f32 %0, %0, %14, %15\n\tv_max_f32 %0, %0, %16"
;       : "=&v"(b) : "v"(a), "v"(p1[1]), "v"(p1[2]), "v"(p1[3]), "v"(p1[4]), "v"(p1[5]), "v"(p1[6]), "v"(p1[7]), "v"(p1[8]), "v"(p1[9]), "v"(p1[10]), "v"(p1[11]), "v"(p1[12]), "v"(p1[13]), "v"(p1[14]), "v"(p1[15]));
;   return b;
;     ...
;   for (int t = 0; t + 1 < NT; ++t) {
;     if constexpr (ABL & 1) { u32x4 w0 = {cvtpk(p0[0], p0[1]), cvtpk(p0[2], p0[3]), cvtpk(p0[4], p0[5]), cvtpk(p0[6], p0[7])}, w1 = {cvtpk(p0[8], p0[9]), cvtpk(p0[10], p0[11]), cvtpk(p0[12], p0[13]), cvtpk(p0[14], p0[15])};
;         u32x4 w2 = {cvtpk(p1[0], p1[1]), cvtpk(p1[2], p1[3]), cvtpk(p1[4], p1[5]), cvtpk(p1[6], p1[7])}, w3 = {cvtpk(p1[8], p1[9]), cvtpk(p1[10], p1[11]), cvtpk(p1[12], p1[13]), cvtpk(p1[14], p1[15])};
;         pa0 = *reinterpret_cast<bf16x8*>(&w0); pa1 = *reinterpret_cast<bf16x8*>(&w1); pa2 = *reinterpret_cast<bf16x8*>(&w2); pa3 = *reinterpret_cast<bf16x8*>(&w3); }
;     else { ATT_SOFTMAX(t == 0); }
;     if constexpr (!(ABL & 4)) { ATT_WRITE_K(k2); ATT_WRITE_V(v1); }
;     ATT_SBAR();
; #pragma unroll
;     for (int ks = 0; ks < 4; ++ks) ATT_VPAIR(va, v0, 0, ks);
;     asm volatile("s_waitcnt lgkmcnt(8)" ::: "memory"); ATT_BAR();
;     ATT_XSECTION(true);
;     if constexpr (!(ABL & 4)) { const int tk = (t + 3 < NT) ? t + 3 : NT - 1, tv = (t + 2 < NT) ? t + 2 : NT - 1; ATT_LOAD_K(tk); ATT_LOAD_V(tv); }
;     ATT_BAR();
;     { const int tk_ = k0; k0 = k1; k1 = k2; k2 = tk_; const int tv_ = v0; v0 = v1; v1 = v2; v2 = tv_; }
	s_setprio 2
	s_waitcnt lgkmcnt(3)
	v_mfma_f32_32x32x16_bf16 v[98:113], v[152:155], v[136:139], v[82:97]
	ds_read_b128 v[180:183], v249 offset:34880
	s_waitcnt lgkmcnt(3)
	v_mfma_f32_32x32x16_bf16 v[114:129], v[156:159], v[136:139], v[82:97]
	ds_read_b128 v[186:189], v249 offset:39488
	s_waitcnt lgkmcnt(3)
	v_mfma_f32_32x32x16_bf16 v[98:113], v[160:163], v[140:143], v[98:113]
	ds_read_b128 v[190:193], v249 offset:34912
	ds_read_b64_tr_b16 v[198:199], v131 offset:16384
	ds_read_b64_tr_b16 v[200:201], v131 offset:18432
	s_waitcnt lgkmcnt(5)
	v_mfma_f32_32x32x16_bf16 v[114:129], v[176:179], v[140:143], v[114:129]
	ds_read_b128 v[194:197], v249 offset:39520
	ds_read_b64_tr_b16 v[212:213], v131 offset:20480
	ds_read_b64_tr_b16 v[214:215], v131 offset:22528
	s_waitcnt lgkmcnt(7)
	v_mfma_f32_32x32x16_bf16 v[98:113], v[180:183], v[144:147], v[98:113]
	ds_read_b64_tr_b16 v[216:217], v131 offset:24576
	ds_read_b64_tr_b16 v[218:219], v131 offset:26624
	s_waitcnt lgkmcnt(8)
	v_mfma_f32_32x32x16_bf16 v[114:129], v[186:189], v[144:147], v[114:129]
	ds_read_b64_tr_b16 v[220:221], v131 offset:28672
	ds_read_b64_tr_b16 v[222:223], v131 offset:30720
	s_waitcnt lgkmcnt(9)
	v_mfma_f32_32x32x16_bf16 v[98:113], v[190:193], v[148:151], v[98:113]
	s_waitcnt lgkmcnt(6)
	v_mfma_f32_32x32x16_bf16 v[114:129], v[194:197], v[148:151], v[114:129]
	v_mfma_f32_32x32x16_bf16 v[18:33], v[2:5], v[198:201], v[18:33]
	ds_read_b64_tr_b16 v[236:237], v131 offset:16896
	ds_read_b64_tr_b16 v[238:239], v131 offset:18944
	s_waitcnt lgkmcnt(6)
	v_mfma_f32_32x32x16_bf16 v[18:33], v[6:9], v[212:215], v[18:33]
	ds_read_b64_tr_b16 v[198:199], v131 offset:20992
	ds_read_b64_tr_b16 v[200:201], v131 offset:23040
	s_waitcnt lgkmcnt(6)
	v_mfma_f32_32x32x16_bf16 v[18:33], v[10:13], v[216:219], v[18:33]
	ds_read_b64_tr_b16 v[212:213], v131 offset:25088
	ds_read_b64_tr_b16 v[214:215], v131 offset:27136
	s_waitcnt lgkmcnt(6)
	v_mfma_f32_32x32x16_bf16 v[18:33], v[14:17], v[220:223], v[18:33]
	ds_read_b64_tr_b16 v[216:217], v131 offset:29184
	ds_read_b64_tr_b16 v[218:219], v131 offset:31232
	v_max3_f32 v152, v98, v99, v100
	s_waitcnt lgkmcnt(6)
	v_mfma_f32_32x32x16_bf16 v[34:49], v[2:5], v[236:239], v[34:49]
	ds_read_b64_tr_b16 v[220:221], v131 offset:17408
	ds_read_b64_tr_b16 v[222:223], v131 offset:19456
	v_max3_f32 v173, v114, v115, v116
	s_waitcnt lgkmcnt(6)
	v_mfma_f32_32x32x16_bf16 v[34:49], v[6:9], v[198:201], v[34:49]
	ds_read_b64_tr_b16 v[236:237], v131 offset:21504
	ds_read_b64_tr_b16 v[238:239], v131 offset:23552
	v_max3_f32 v152, v152, v101, v102
	s_waitcnt lgkmcnt(6)
	v_mfma_f32_32x32x16_bf16 v[34:49], v[10:13], v[212:215], v[34:49]
	ds_read_b64_tr_b16 v[198:199], v131 offset:25600
	ds_read_b64_tr_b16 v[200:201], v131 offset:27648
	v_max3_f32 v173, v173, v117, v118
	s_waitcnt lgkmcnt(6)
	v_mfma_f32_32x32x16_bf16 v[34:49], v[14:17], v[216:219], v[34:49]
	ds_read_b64_tr_b16 v[212:213], v131 offset:29696
	ds_read_b64_tr_b16 v[214:215], v131 offset:31744
	v_max3_f32 v152, v152, v103, v104
	s_waitcnt lgkmcnt(6)
	v_mfma_f32_32x32x16_bf16 v[50:65], v[2:5], v[220:223], v[50:65]
	ds_read_b64_tr_b16 v[216:217], v131 offset:17920
	ds_read_b64_tr_b16 v[218:219], v131 offset:19968
	v_max3_f32 v173, v173, v119, v120
	s_waitcnt lgkmcnt(6)
	v_mfma_f32_32x32x16_bf16 v[50:65], v[6:9], v[236:239], v[50:65]
	ds_read_b64_tr_b16 v[220:221], v131 offset:22016
	ds_read_b64_tr_b16 v[222:223], v131 offset:24064
	v_max3_f32 v152, v152, v105, v106
	s_waitcnt lgkmcnt(6)
	v_mfma_f32_32x32x16_bf16 v[50:65], v[10:13], v[198:201], v[50:65]
	ds_read_b64_tr_b16 v[236:237], v131 offset:26112
	ds_read_b64_tr_b16 v[238:239], v131 offset:28160
	v_max3_f32 v173, v173, v121, v122
	s_waitcnt lgkmcnt(6)
	v_mfma_f32_32x32x16_bf16 v[50:65], v[14:17], v[212:215], v[50:65]
	ds_read_b64_tr_b16 v[198:199], v131 offset:30208
	ds_read_b64_tr_b16 v[200:201], v131 offset:32256
	v_max3_f32 v152, v152, v107, v108
	s_waitcnt lgkmcnt(6)
	v_mfma_f32_32x32x16_bf16 v[66:81], v[2:5], v[216:219], v[66:81]
	v_max3_f32 v173, v173, v123, v124
	s_min_u32 s14, s97, 0x7c
	s_lshl_b32 s14, s14, 17
	s_add_i32 s14, s14, 0x60000
	buffer_load_dwordx4 v[224:227], v170, s[8:11], s14 offen
	s_waitcnt lgkmcnt(4)
	v_mfma_f32_32x32x16_bf16 v[66:81], v[6:9], v[220:223], v[66:81]
	v_max3_f32 v152, v152, v109, v110
	s_add_i32 s19, s36, 0xffff0000
	s_mov_b32 s14, s10
	s_mov_b32 s15, s11
	buffer_load_dwordx4 v[228:231], v171, s[12:15], s19 offen
	s_waitcnt lgkmcnt(2)
	v_mfma_f32_32x32x16_bf16 v[66:81], v[10:13], v[236:239], v[66:81]
	v_max3_f32 v173, v173, v125, v126
	buffer_load_dwordx4 v[232:235], v171, s[12:15], s36 offen
	s_waitcnt lgkmcnt(0)
	v_mfma_f32_32x32x16_bf16 v[66:81], v[14:17], v[198:201], v[66:81]
	v_max3_f32 v152, v152, v111, v112
	v_mfma_f32_4x4x4_16b_bf16 v[240:243], v[2:3], v[132:133], v[240:243]
	v_max3_f32 v173, v173, v127, v128
	v_mfma_f32_4x4x4_16b_bf16 v[244:247], v[4:5], v[132:133], v[244:247]
	v_mfma_f32_4x4x4_16b_bf16 v[240:243], v[6:7], v[132:133], v[240:243]
	v_max_f32 v152, v152, v113
	v_mfma_f32_4x4x4_16b_bf16 v[244:247], v[8:9], v[132:133], v[244:247]
	v_mfma_f32_4x4x4_16b_bf16 v[240:243], v[10:11], v[132:133], v[240:243]
	v_max_f32 v173, v173, v129
	v_mfma_f32_4x4x4_16b_bf16 v[244:247], v[12:13], v[132:133], v[244:247]
	v_mfma_f32_4x4x4_16b_bf16 v[240:243], v[14:15], v[132:133], v[240:243]
	v_max_f32 v173, v173, v152
	v_mfma_f32_4x4x4_16b_bf16 v[244:247], v[16:17], v[132:133], v[244:247]
	s_setprio 0
	s_barrier
	s_add_i32 s36, s36, 0x20000
	s_add_i32 s97, s97, 1
	s_cmpk_eq_i32 s97, 0x7e
	s_cbranch_scc1 .Lu3_exit_b1_0

; #define ATT_SBAR() __builtin_amdgcn_sched_barrier(0)
; #define ATT_PK4(P, BASE, OUT) do { u32x4 w = {cvtpk(P[BASE + 0], P[BASE + 1]), cvtpk(P[BASE + 2], P[BASE + 3]), cvtpk(P[BASE + 4], P[BASE + 5]), cvtpk(P[BASE + 6], P[BASE + 7])}; \
;     OUT = *reinterpret_cast<bf16x8*>(&w); } while (0)
; #define ATT_WRITE_K(so) do { *(bf16x8*)(K_lds + (so) + kswz<DQK>(kr, kc * 2)) = sk0; if constexpr (DQK == 128) *(bf16x8*)(K_lds + (so) + kswz<DQK>(32 + kr, kc * 2)) = sk1; } while (0)
; #define ATT_WRITE_V(so) do { *(bf16x8*)(V_lds + (so) + vst0) = sv0; *(bf16x8*)(V_lds + (so) + vst1) = sv1; } while (0)
; #define ATT_BAR() do { ATT_SBAR(); asm volatile("s_barrier" ::: "memory"); ATT_SBAR(); } while (0)
; #define ATT_VPAIR(buf, so, blk, ks) do { if constexpr (!(ABL & 8) && !(ABL & 32)) { buf[2 * (ks)] = vtr(vq0 + (so) + v_rd_off(blk, ks, 0)); buf[2 * (ks) + 1] = vtr(vq0 + (so) + v_rd_off(blk, ks, 1)); } } while (0)
; __device__ __forceinline__ void softmax_exp_pack(f32x16& p0, f32x16& p1, bf16x8& pa0, bf16x8& pa1, bf16x8& pa2, bf16x8& pa3) {
; #pragma unroll
;   for (int r = 0; r < 16; ++r) { p0[r] = __builtin_amdgcn_exp2f(p0[r]); p1[r] = __builtin_amdgcn_exp2f(p1[r]); }
;     ...
;   ATT_PK4(p0, 0, pa0); ATT_PK4(p0, 8, pa1); ATT_PK4(p1, 0, pa2); ATT_PK4(p1, 8, pa3);
;     ...
;     if constexpr (!(ABL & 4)) { ATT_WRITE_K(k2); ATT_WRITE_V(v1); }
;     ATT_SBAR();
; #pragma unroll
;     for (int ks = 0; ks < 4; ++ks) ATT_VPAIR(va, v0, 0, ks);
;     asm volatile("s_waitcnt lgkmcnt(8)" ::: "memory"); ATT_BAR();
.Lu3_join_b1_1:
	v_exp_f32_e32 v98, v98
	v_exp_f32_e32 v114, v114
	v_exp_f32_e32 v99, v99
	v_exp_f32_e32 v115, v115
	v_exp_f32_e32 v100, v100
	v_exp_f32_e32 v101, v101
	v_exp_f32_e32 v102, v102
	v_exp_f32_e32 v103, v103
	v_exp_f32_e32 v106, v106
	v_exp_f32_e32 v107, v107
	v_exp_f32_e32 v116, v116
	v_exp_f32_e32 v117, v117
	v_exp_f32_e32 v118, v118
	v_exp_f32_e32 v119, v119
	v_exp_f32_e32 v104, v104
	v_exp_f32_e32 v120, v120
	v_exp_f32_e32 v105, v105
	v_exp_f32_e32 v121, v121
	v_exp_f32_e32 v122, v122
	v_exp_f32_e32 v123, v123
	v_exp_f32_e32 v108, v108
	v_exp_f32_e32 v124, v124
	v_exp_f32_e32 v109, v109
	v_exp_f32_e32 v125, v125
	v_exp_f32_e32 v110, v110
	v_exp_f32_e32 v126, v126
	v_exp_f32_e32 v111, v111
	v_exp_f32_e32 v127, v127
	v_exp_f32_e32 v112, v112
	v_exp_f32_e32 v128, v128
	v_exp_f32_e32 v113, v113
	v_exp_f32_e32 v129, v129
	v_cvt_pk_bf16_f32 v2, v98, v99
	v_cvt_pk_bf16_f32 v3, v100, v101
	v_cvt_pk_bf16_f32 v4, v102, v103
	v_cvt_pk_bf16_f32 v6, v106, v107
	v_cvt_pk_bf16_f32 v10, v114, v115
	v_cvt_pk_bf16_f32 v5, v104, v105
	v_cvt_pk_bf16_f32 v7, v108, v109
	v_cvt_pk_bf16_f32 v8, v110, v111
	v_cvt_pk_bf16_f32 v9, v112, v113
	v_cvt_pk_bf16_f32 v11, v116, v117
	v_cvt_pk_bf16_f32 v12, v118, v119
	v_cvt_pk_bf16_f32 v13, v120, v121
	v_cvt_pk_bf16_f32 v14, v122, v123
	v_cvt_pk_bf16_f32 v15, v124, v125
	v_cvt_pk_bf16_f32 v16, v126, v127
	v_cvt_pk_bf16_f32 v17, v128, v129
	s_waitcnt vmcnt(0)
	ds_write_b128 v248, v[224:227] offset:25600
	ds_write_b128 v167, v[228:231]
	ds_write_b128 v168, v[232:235]
	ds_read_b128 v[152:155], v249 offset:16384
	ds_read_b128 v[156:159], v249 offset:20992
	ds_read_b128 v[160:163], v249 offset:16416
	ds_read_b128 v[176:179], v249 offset:21024
	s_waitcnt lgkmcnt(4)
	s_barrier
; #define ATT_SBAR() __builtin_amdgcn_sched_barrier(0)
; __device__ __forceinline__ float softmax_rowmax(const f32x16& p0, const f32x16& p1) {
;   const float m0 = p1[0] + 0.0f; float a, b;
;   asm("v_max3_f32 %0, %1, %2, %3\n\tv_max3_f32 %0, %0, %4, %5\n\tv_max3_f32 %0, %0, %6, %7\n\tv_max3_f32 %0, %0, %8, %9\n\t"
;       "v_max3_f32 %0, %0, %10, %11\n\tv_max3_f32 %0, %0, %12, %13\n\tv_max3_f32 %0, %0, %14, %15\n\tv_max3_f32 %0, %0, %16, %17"
;       : "=&v"(a) : "v"(m0), "v"(p0[0]), "v"(p0[1]), "v"(p0[2]), "v"(p0[3]), "v"(p0[4]), "v"(p0[5]), "v"(p0[6]), "v"(p0[7]), "v"(p0[8]), "v"(p0[9]), "v"(p0[10]), "v"(p0[11]), "v"(p0[12]), "v"(p0[13]), "v"(p0[14]), "v"(p0[15]));
;   asm("v_max3_f32 %0, %1, %2, %3\n\tv_max3_f32 %0, %0, %4, %5\n\tv_max3_f32 %0, %0, %6, %7\n\tv_max3_f32 %0, %0, %8, %9\n\t"
;       "v_max3_f32 %0, %0, %10, %11\n\tv_max3_f32 %0, %0, %12, %13\n\tv_max3_f32 %0, %0, %14, %15\n\tv_max_f32 %0, %0, %16"
;       : "=&v"(b) : "v"(a), "v"(p1[1]), "v"(p1[2]), "v"(p1[3]), "v"(p1[4]), "v"(p1[5]), "v"(p1[6]), "v"(p1[7]), "v"(p1[8]), "v"(p1[9]), "v"(p1[10]), "v"(p1[11]), "v"(p1[12]), "v"(p1[13]), "v"(p1[14]), "v"(p1[15]));
;   return b;
;     ...
;   for (int t = 0; t + 1 < NT; ++t) {
;     if constexpr (ABL & 1) { u32x4 w0 = {cvtpk(p0[0], p0[1]), cvtpk(p0[2], p0[3]), cvtpk(p0[4], p0[5]), cvtpk(p0[6], p0[7])}, w1 = {cvtpk(p0[8], p0[9]), cvtpk(p0[10], p0[11]), cvtpk(p0[12], p0[13]), cvtpk(p0[14], p0[15])};
;         u32x4 w2 = {cvtpk(p1[0], p1[1]), cvtpk(p1[2], p1[3]), cvtpk(p1[4], p1[5]), cvtpk(p1[6], p1[7])}, w3 = {cvtpk(p1[8], p1[9]), cvtpk(p1[10], p1[11]), cvtpk(p1[12], p1[13]), cvtpk(p1[14], p1[15])};
;         pa0 = *reinterpret_cast<bf16x8*>(&w0); pa1 = *reinterpret_cast<bf16x8*>(&w1); pa2 = *reinterpret_cast<bf16x8*>(&w2); pa3 = *reinterpret_cast<bf16x8*>(&w3); }
;     else { ATT_SOFTMAX(t == 0); }
;     if constexpr (!(ABL & 4)) { ATT_WRITE_K(k2); ATT_WRITE_V(v1); }
;     ATT_SBAR();
; #pragma unroll
;     for (int ks = 0; ks < 4; ++ks) ATT_VPAIR(va, v0, 0, ks);
;     asm volatile("s_waitcnt lgkmcnt(8)" ::: "memory"); ATT_BAR();
;     ATT_XSECTION(true);
;     if constexpr (!(ABL & 4)) { const int tk = (t + 3 < NT) ? t + 3 : NT - 1, tv = (t + 2 < NT) ? t + 2 : NT - 1; ATT_LOAD_K(tk); ATT_LOAD_V(tv); }
;     ATT_BAR();
;     { const int tk_ = k0; k0 = k1; k1 = k2; k2 = tk_; const int tv_ = v0; v0 = v1; v1 = v2; v2 = tv_; }
	s_setprio 2
	s_waitcnt lgkmcnt(3)
	v_mfma_f32_32x32x16_bf16 v[98:113], v[152:155], v[136:139], v[82:97]
	ds_read_b128 v[180:183], v249 offset:16448
	s_waitcnt lgkmcnt(3)
	v_mfma_f32_32x32x16_bf16 v[114:129], v[156:159], v[136:139], v[82:97]
	ds_read_b128 v[186:189], v249 offset:21056
	s_waitcnt lgkmcnt(3)
	v_mfma_f32_32x32x16_bf16 v[98:113], v[160:163], v[140:143], v[98:113]
	ds_read_b128 v[190:193], v249 offset:16480
	ds_read_b64_tr_b16 v[198:199], v131 offset:32768
	ds_read_b64_tr_b16 v[200:201], v131 offset:34816
	s_waitcnt lgkmcnt(5)
	v_mfma_f32_32x32x16_bf16 v[114:129], v[176:179], v[140:143], v[114:129]
	ds_read_b128 v[194:197], v249 offset:21088
	ds_read_b64_tr_b16 v[212:213], v131 offset:36864
	ds_read_b64_tr_b16 v[214:215], v131 offset:38912
	s_waitcnt lgkmcnt(7)
	v_mfma_f32_32x32x16_bf16 v[98:113], v[180:183], v[144:147], v[98:113]
	ds_read_b64_tr_b16 v[216:217], v131 offset:40960
	ds_read_b64_tr_b16 v[218:219], v131 offset:43008
	s_waitcnt lgkmcnt(8)
	v_mfma_f32_32x32x16_bf16 v[114:129], v[186:189], v[144:147], v[114:129]
	ds_read_b64_tr_b16 v[220:221], v131 offset:45056
	ds_read_b64_tr_b16 v[222:223], v131 offset:47104
	s_waitcnt lgkmcnt(9)
	v_mfma_f32_32x32x16_bf16 v[98:113], v[190:193], v[148:151], v[98:113]
	s_waitcnt lgkmcnt(6)
	v_mfma_f32_32x32x16_bf16 v[114:129], v[194:197], v[148:151], v[114:129]
	v_mfma_f32_32x32x16_bf16 v[18:33], v[2:5], v[198:201], v[18:33]
	ds_read_b64_tr_b16 v[236:237], v131 offset:33280
	ds_read_b64_tr_b16 v[238:239], v131 offset:35328
	s_waitcnt lgkmcnt(6)
	v_mfma_f32_32x32x16_bf16 v[18:33], v[6:9], v[212:215], v[18:33]
	ds_read_b64_tr_b16 v[198:199], v131 offset:37376
	ds_read_b64_tr_b16 v[200:201], v131 offset:39424
	s_waitcnt lgkmcnt(6)
	v_mfma_f32_32x32x16_bf16 v[18:33], v[10:13], v[216:219], v[18:33]
	ds_read_b64_tr_b16 v[212:213], v131 offset:41472
	ds_read_b64_tr_b16 v[214:215], v131 offset:43520
	s_waitcnt lgkmcnt(6)
	v_mfma_f32_32x32x16_bf16 v[18:33], v[14:17], v[220:223], v[18:33]
	ds_read_b64_tr_b16 v[216:217], v131 offset:45568
	ds_read_b64_tr_b16 v[218:219], v131 offset:47616
	v_max3_f32 v152, v98, v99, v100
	s_waitcnt lgkmcnt(6)
	v_mfma_f32_32x32x16_bf16 v[34:49], v[2:5], v[236:239], v[34:49]
	ds_read_b64_tr_b16 v[220:221], v131 offset:33792
	ds_read_b64_tr_b16 v[222:223], v131 offset:35840
	v_max3_f32 v173, v114, v115, v116
	s_waitcnt lgkmcnt(6)
	v_mfma_f32_32x32x16_bf16 v[34:49], v[6:9], v[198:201], v[34:49]
	ds_read_b64_tr_b16 v[236:237], v131 offset:37888
	ds_read_b64_tr_b16 v[238:239], v131 offset:39936
	v_max3_f32 v152, v152, v101, v102
	s_waitcnt lgkmcnt(6)
	v_mfma_f32_32x32x16_bf16 v[34:49], v[10:13], v[212:215], v[34:49]
	ds_read_b64_tr_b16 v[198:199], v131 offset:41984
	ds_read_b64_tr_b16 v[200:201], v131 offset:44032
	v_max3_f32 v173, v173, v117, v118
	s_waitcnt lgkmcnt(6)
	v_mfma_f32_32x32x16_bf16 v[34:49], v[14:17], v[216:219], v[34:49]
	ds_read_b64_tr_b16 v[212:213], v131 offset:46080
	ds_read_b64_tr_b16 v[214:215], v131 offset:48128
	v_max3_f32 v152, v152, v103, v104
	s_waitcnt lgkmcnt(6)
	v_mfma_f32_32x32x16_bf16 v[50:65], v[2:5], v[220:223], v[50:65]
	ds_read_b64_tr_b16 v[216:217], v131 offset:34304
	ds_read_b64_tr_b16 v[218:219], v131 offset:36352
	v_max3_f32 v173, v173, v119, v120
	s_waitcnt lgkmcnt(6)
	v_mfma_f32_32x32x16_bf16 v[50:65], v[6:9], v[236:239], v[50:65]
	ds_read_b64_tr_b16 v[220:221], v131 offset:38400
	ds_read_b64_tr_b16 v[222:223], v131 offset:40448
	v_max3_f32 v152, v152, v105, v106
	s_waitcnt lgkmcnt(6)
	v_mfma_f32_32x32x16_bf16 v[50:65], v[10:13], v[198:201], v[50:65]
	ds_read_b64_tr_b16 v[236:237], v131 offset:42496
	ds_read_b64_tr_b16 v[238:239], v131 offset:44544
	v_max3_f32 v173, v173, v121, v122
	s_waitcnt lgkmcnt(6)
	v_mfma_f32_32x32x16_bf16 v[50:65], v[14:17], v[212:215], v[50:65]
	ds_read_b64_tr_b16 v[198:199], v131 offset:46592
	ds_read_b64_tr_b16 v[200:201], v131 offset:48640
	v_max3_f32 v152, v152, v107, v108
	s_waitcnt lgkmcnt(6)
	v_mfma_f32_32x32x16_bf16 v[66:81], v[2:5], v[216:219], v[66:81]
	v_max3_f32 v173, v173, v123, v124
	s_min_u32 s14, s97, 0x7c
	s_lshl_b32 s14, s14, 17
	s_add_i32 s14, s14, 0x60000
	buffer_load_dwordx4 v[224:227], v170, s[8:11], s14 offen
	s_waitcnt lgkmcnt(4)
	v_mfma_f32_32x32x16_bf16 v[66:81], v[6:9], v[220:223], v[66:81]
	v_max3_f32 v152, v152, v109, v110
	s_add_i32 s19, s36, 0xffff0000
	s_mov_b32 s14, s10
	s_mov_b32 s15, s11
	buffer_load_dwordx4 v[228:231], v171, s[12:15], s19 offen
	s_waitcnt lgkmcnt(2)
	v_mfma_f32_32x32x16_bf16 v[66:81], v[10:13], v[236:239], v[66:81]
	v_max3_f32 v173, v173, v125, v126
	buffer_load_dwordx4 v[232:235], v171, s[12:15], s36 offen
	s_waitcnt lgkmcnt(0)
	v_mfma_f32_32x32x16_bf16 v[66:81], v[14:17], v[198:201], v[66:81]
	v_max3_f32 v152, v152, v111, v112
	v_mfma_f32_4x4x4_16b_bf16 v[240:243], v[2:3], v[132:133], v[240:243]
	v_max3_f32 v173, v173, v127, v128
	v_mfma_f32_4x4x4_16b_bf16 v[244:247], v[4:5], v[132:133], v[244:247]
	v_mfma_f32_4x4x4_16b_bf16 v[240:243], v[6:7], v[132:133], v[240:243]
	v_max_f32 v152, v152, v113
	v_mfma_f32_4x4x4_16b_bf16 v[244:247], v[8:9], v[132:133], v[244:247]
	v_mfma_f32_4x4x4_16b_bf16 v[240:243], v[10:11], v[132:133], v[240:243]
	v_max_f32 v173, v173, v129
	v_mfma_f32_4x4x4_16b_bf16 v[244:247], v[12:13], v[132:133], v[244:247]
	v_mfma_f32_4x4x4_16b_bf16 v[240:243], v[14:15], v[132:133], v[240:243]
	v_max_f32 v173, v173, v152
	v_mfma_f32_4x4x4_16b_bf16 v[244:247], v[16:17], v[132:133], v[244:247]
	s_setprio 0
	s_barrier
	s_add_i32 s36, s36, 0x20000
	s_add_i32 s97, s97, 1
	s_cmpk_eq_i32 s97, 0x7e
	s_cbranch_scc1 .Lu3_exit_b1_1

; #define ATT_SBAR() __builtin_amdgcn_sched_barrier(0)
; #define ATT_PK4(P, BASE, OUT) do { u32x4 w = {cvtpk(P[BASE + 0], P[BASE + 1]), cvtpk(P[BASE + 2], P[BASE + 3]), cvtpk(P[BASE + 4], P[BASE + 5]), cvtpk(P[BASE + 6], P[BASE + 7])}; \
;     OUT = *reinterpret_cast<bf16x8*>(&w); } while (0)
; #define ATT_WRITE_K(so) do { *(bf16x8*)(K_lds + (so) + kswz<DQK>(kr, kc * 2)) = sk0; if constexpr (DQK == 128) *(bf16x8*)(K_lds + (so) + kswz<DQK>(32 + kr, kc * 2)) = sk1; } while (0)
; #define ATT_WRITE_V(so) do { *(bf16x8*)(V_lds + (so) + vst0) = sv0; *(bf16x8*)(V_lds + (so) + vst1) = sv1; } while (0)
; #define ATT_BAR() do { ATT_SBAR(); asm volatile("s_barrier" ::: "memory"); ATT_SBAR(); } while (0)
; #define ATT_VPAIR(buf, so, blk, ks) do { if constexpr (!(ABL & 8) && !(ABL & 32)) { buf[2 * (ks)] = vtr(vq0 + (so) + v_rd_off(blk, ks, 0)); buf[2 * (ks) + 1] = vtr(vq0 + (so) + v_rd_off(blk, ks, 1)); } } while (0)
; __device__ __forceinline__ void softmax_exp_pack(f32x16& p0, f32x16& p1, bf16x8& pa0, bf16x8& pa1, bf16x8& pa2, bf16x8& pa3) {
; #pragma unroll
;   for (int r = 0; r < 16; ++r) { p0[r] = __builtin_amdgcn_exp2f(p0[r]); p1[r] = __builtin_amdgcn_exp2f(p1[r]); }
;     ...
;   ATT_PK4(p0, 0, pa0); ATT_PK4(p0, 8, pa1); ATT_PK4(p1, 0, pa2); ATT_PK4(p1, 8, pa3);
;     ...
;     if constexpr (!(ABL & 4)) { ATT_WRITE_K(k2); ATT_WRITE_V(v1); }
;     ATT_SBAR();
; #pragma unroll
;     for (int ks = 0; ks < 4; ++ks) ATT_VPAIR(va, v0, 0, ks);
;     asm volatile("s_waitcnt lgkmcnt(8)" ::: "memory"); ATT_BAR();
.Lu3_join_b1_2:
	v_exp_f32_e32 v98, v98
	v_exp_f32_e32 v114, v114
	v_exp_f32_e32 v99, v99
	v_exp_f32_e32 v115, v115
	v_exp_f32_e32 v100, v100
	v_exp_f32_e32 v101, v101
	v_exp_f32_e32 v102, v102
	v_exp_f32_e32 v103, v103
	v_exp_f32_e32 v106, v106
	v_exp_f32_e32 v107, v107
	v_exp_f32_e32 v116, v116
	v_exp_f32_e32 v117, v117
	v_exp_f32_e32 v118, v118
	v_exp_f32_e32 v119, v119
	v_exp_f32_e32 v104, v104
	v_exp_f32_e32 v120, v120
	v_exp_f32_e32 v105, v105
	v_exp_f32_e32 v121, v121
	v_exp_f32_e32 v122, v122
	v_exp_f32_e32 v123, v123
	v_exp_f32_e32 v108, v108
	v_exp_f32_e32 v124, v124
	v_exp_f32_e32 v109, v109
	v_exp_f32_e32 v125, v125
	v_exp_f32_e32 v110, v110
	v_exp_f32_e32 v126, v126
	v_exp_f32_e32 v111, v111
	v_exp_f32_e32 v127, v127
	v_exp_f32_e32 v112, v112
	v_exp_f32_e32 v128, v128
	v_exp_f32_e32 v113, v113
	v_exp_f32_e32 v129, v129
	v_cvt_pk_bf16_f32 v2, v98, v99
	v_cvt_pk_bf16_f32 v3, v100, v101
	v_cvt_pk_bf16_f32 v4, v102, v103
	v_cvt_pk_bf16_f32 v6, v106, v107
	v_cvt_pk_bf16_f32 v10, v114, v115
	v_cvt_pk_bf16_f32 v5, v104, v105
	v_cvt_pk_bf16_f32 v7, v108, v109
	v_cvt_pk_bf16_f32 v8, v110, v111
	v_cvt_pk_bf16_f32 v9, v112, v113
	v_cvt_pk_bf16_f32 v11, v116, v117
	v_cvt_pk_bf16_f32 v12, v118, v119
	v_cvt_pk_bf16_f32 v13, v120, v121
	v_cvt_pk_bf16_f32 v14, v122, v123
	v_cvt_pk_bf16_f32 v15, v124, v125
	v_cvt_pk_bf16_f32 v16, v126, v127
	v_cvt_pk_bf16_f32 v17, v128, v129
	s_waitcnt vmcnt(0)
	ds_write_b128 v248, v[224:227] offset:34816
	ds_write_b128 v167, v[228:231] offset:16384
	ds_write_b128 v168, v[232:235] offset:16384
	ds_read_b128 v[152:155], v249 offset:25600
	ds_read_b128 v[156:159], v249 offset:30208
	ds_read_b128 v[160:163], v249 offset:25632
	ds_read_b128 v[176:179], v249 offset:30240
	s_waitcnt lgkmcnt(4)
	s_barrier
; #define ATT_SBAR() __builtin_amdgcn_sched_barrier(0)
; __device__ __forceinline__ float softmax_rowmax(const f32x16& p0, const f32x16& p1) {
;   const float m0 = p1[0] + 0.0f; float a, b;
;   asm("v_max3_f32 %0, %1, %2, %3\n\tv_max3_f32 %0, %0, %4, %5\n\tv_max3_f32 %0, %0, %6, %7\n\tv_max3_f32 %0, %0, %8, %9\n\t"
;       "v_max3_f32 %0, %0, %10, %11\n\tv_max3_f32 %0, %0, %12, %13\n\tv_max3_f32 %0, %0, %14, %15\n\tv_max3_f32 %0, %0, %16, %17"
;       : "=&v"(a) : "v"(m0), "v"(p0[0]), "v"(p0[1]), "v"(p0[2]), "v"(p0[3]), "v"(p0[4]), "v"(p0[5]), "v"(p0[6]), "v"(p0[7]), "v"(p0[8]), "v"(p0[9]), "v"(p0[10]), "v"(p0[11]), "v"(p0[12]), "v"(p0[13]), "v"(p0[14]), "v"(p0[15]));
;   asm("v_max3_f32 %0, %1, %2, %3\n\tv_max3_f32 %0, %0, %4, %5\n\tv_max3_f32 %0, %0, %6, %7\n\tv_max3_f32 %0, %0, %8, %9\n\t"
;       "v_max3_f32 %0, %0, %10, %11\n\tv_max3_f32 %0, %0, %12, %13\n\tv_max3_f32 %0, %0, %14, %15\n\tv_max_f32 %0, %0, %16"
;       : "=&v"(b) : "v"(a), "v"(p1[1]), "v"(p1[2]), "v"(p1[3]), "v"(p1[4]), "v"(p1[5]), "v"(p1[6]), "v"(p1[7]), "v"(p1[8]), "v"(p1[9]), "v"(p1[10]), "v"(p1[11]), "v"(p1[12]), "v"(p1[13]), "v"(p1[14]), "v"(p1[15]));
;   return b;
;     ...
;   for (int t = 0; t + 1 < NT; ++t) {
;     if constexpr (ABL & 1) { u32x4 w0 = {cvtpk(p0[0], p0[1]), cvtpk(p0[2], p0[3]), cvtpk(p0[4], p0[5]), cvtpk(p0[6], p0[7])}, w1 = {cvtpk(p0[8], p0[9]), cvtpk(p0[10], p0[11]), cvtpk(p0[12], p0[13]), cvtpk(p0[14], p0[15])};
;         u32x4 w2 = {cvtpk(p1[0], p1[1]), cvtpk(p1[2], p1[3]), cvtpk(p1[4], p1[5]), cvtpk(p1[6], p1[7])}, w3 = {cvtpk(p1[8], p1[9]), cvtpk(p1[10], p1[11]), cvtpk(p1[12], p1[13]), cvtpk(p1[14], p1[15])};
;         pa0 = *reinterpret_cast<bf16x8*>(&w0); pa1 = *reinterpret_cast<bf16x8*>(&w1); pa2 = *reinterpret_cast<bf16x8*>(&w2); pa3 = *reinterpret_cast<bf16x8*>(&w3); }
;     else { ATT_SOFTMAX(t == 0); }
;     if constexpr (!(ABL & 4)) { ATT_WRITE_K(k2); ATT_WRITE_V(v1); }
;     ATT_SBAR();
; #pragma unroll
;     for (int ks = 0; ks < 4; ++ks) ATT_VPAIR(va, v0, 0, ks);
;     asm volatile("s_waitcnt lgkmcnt(8)" ::: "memory"); ATT_BAR();
;     ATT_XSECTION(true);
;     if constexpr (!(ABL & 4)) { const int tk = (t + 3 < NT) ? t + 3 : NT - 1, tv = (t + 2 < NT) ? t + 2 : NT - 1; ATT_LOAD_K(tk); ATT_LOAD_V(tv); }
;     ATT_BAR();
;     { const int tk_ = k0; k0 = k1; k1 = k2; k2 = tk_; const int tv_ = v0; v0 = v1; v1 = v2; v2 = tv_; }
;   }
	s_setprio 2
	s_waitcnt lgkmcnt(3)
	v_mfma_f32_32x32x16_bf16 v[98:113], v[152:155], v[136:139], v[82:97]
	ds_read_b128 v[180:183], v249 offset:25664
	s_waitcnt lgkmcnt(3)
	v_mfma_f32_32x32x16_bf16 v[114:129], v[156:159], v[136:139], v[82:97]
	ds_read_b128 v[186:189], v249 offset:30272
	s_waitcnt lgkmcnt(3)
	v_mfma_f32_32x32x16_bf16 v[98:113], v[160:163], v[140:143], v[98:113]
	ds_read_b128 v[190:193], v249 offset:25696
	ds_read_b64_tr_b16 v[198:199], v131
	ds_read_b64_tr_b16 v[200:201], v131 offset:2048
	s_waitcnt lgkmcnt(5)
	v_mfma_f32_32x32x16_bf16 v[114:129], v[176:179], v[140:143], v[114:129]
	ds_read_b128 v[194:197], v249 offset:30304
	ds_read_b64_tr_b16 v[212:213], v131 offset:4096
	ds_read_b64_tr_b16 v[214:215], v131 offset:6144
	s_waitcnt lgkmcnt(7)
	v_mfma_f32_32x32x16_bf16 v[98:113], v[180:183], v[144:147], v[98:113]
	ds_read_b64_tr_b16 v[216:217], v131 offset:8192
	ds_read_b64_tr_b16 v[218:219], v131 offset:10240
	s_waitcnt lgkmcnt(8)
	v_mfma_f32_32x32x16_bf16 v[114:129], v[186:189], v[144:147], v[114:129]
	ds_read_b64_tr_b16 v[220:221], v131 offset:12288
	ds_read_b64_tr_b16 v[222:223], v131 offset:14336
	s_waitcnt lgkmcnt(9)
	v_mfma_f32_32x32x16_bf16 v[98:113], v[190:193], v[148:151], v[98:113]
	s_waitcnt lgkmcnt(6)
	v_mfma_f32_32x32x16_bf16 v[114:129], v[194:197], v[148:151], v[114:129]
	v_mfma_f32_32x32x16_bf16 v[18:33], v[2:5], v[198:201], v[18:33]
	ds_read_b64_tr_b16 v[236:237], v131 offset:512
	ds_read_b64_tr_b16 v[238:239], v131 offset:2560
	s_waitcnt lgkmcnt(6)
	v_mfma_f32_32x32x16_bf16 v[18:33], v[6:9], v[212:215], v[18:33]
	ds_read_b64_tr_b16 v[198:199], v131 offset:4608
	ds_read_b64_tr_b16 v[200:201], v131 offset:6656
	s_waitcnt lgkmcnt(6)
	v_mfma_f32_32x32x16_bf16 v[18:33], v[10:13], v[216:219], v[18:33]
	ds_read_b64_tr_b16 v[212:213], v131 offset:8704
	ds_read_b64_tr_b16 v[214:215], v131 offset:10752
	s_waitcnt lgkmcnt(6)
	v_mfma_f32_32x32x16_bf16 v[18:33], v[14:17], v[220:223], v[18:33]
	ds_read_b64_tr_b16 v[216:217], v131 offset:12800
	ds_read_b64_tr_b16 v[218:219], v131 offset:14848
	v_max3_f32 v152, v98, v99, v100
	s_waitcnt lgkmcnt(6)
	v_mfma_f32_32x32x16_bf16 v[34:49], v[2:5], v[236:239], v[34:49]
	ds_read_b64_tr_b16 v[220:221], v131 offset:1024
	ds_read_b64_tr_b16 v[222:223], v131 offset:3072
	v_max3_f32 v173, v114, v115, v116
	s_waitcnt lgkmcnt(6)
	v_mfma_f32_32x32x16_bf16 v[34:49], v[6:9], v[198:201], v[34:49]
	ds_read_b64_tr_b16 v[236:237], v131 offset:5120
	ds_read_b64_tr_b16 v[238:239], v131 offset:7168
	v_max3_f32 v152, v152, v101, v102
	s_waitcnt lgkmcnt(6)
	v_mfma_f32_32x32x16_bf16 v[34:49], v[10:13], v[212:215], v[34:49]
	ds_read_b64_tr_b16 v[198:199], v131 offset:9216
	ds_read_b64_tr_b16 v[200:201], v131 offset:11264
	v_max3_f32 v173, v173, v117, v118
	s_waitcnt lgkmcnt(6)
	v_mfma_f32_32x32x16_bf16 v[34:49], v[14:17], v[216:219], v[34:49]
	ds_read_b64_tr_b16 v[212:213], v131 offset:13312
	ds_read_b64_tr_b16 v[214:215], v131 offset:15360
	v_max3_f32 v152, v152, v103, v104
	s_waitcnt lgkmcnt(6)
	v_mfma_f32_32x32x16_bf16 v[50:65], v[2:5], v[220:223], v[50:65]
	ds_read_b64_tr_b16 v[216:217], v131 offset:1536
	ds_read_b64_tr_b16 v[218:219], v131 offset:3584
	v_max3_f32 v173, v173, v119, v120
	s_waitcnt lgkmcnt(6)
	v_mfma_f32_32x32x16_bf16 v[50:65], v[6:9], v[236:239], v[50:65]
	ds_read_b64_tr_b16 v[220:221], v131 offset:5632
	ds_read_b64_tr_b16 v[222:223], v131 offset:7680
	v_max3_f32 v152, v152, v105, v106
	s_waitcnt lgkmcnt(6)
	v_mfma_f32_32x32x16_bf16 v[50:65], v[10:13], v[198:201], v[50:65]
	ds_read_b64_tr_b16 v[236:237], v131 offset:9728
	ds_read_b64_tr_b16 v[238:239], v131 offset:11776
	v_max3_f32 v173, v173, v121, v122
	s_waitcnt lgkmcnt(6)
	v_mfma_f32_32x32x16_bf16 v[50:65], v[14:17], v[212:215], v[50:65]
	ds_read_b64_tr_b16 v[198:199], v131 offset:13824
	ds_read_b64_tr_b16 v[200:201], v131 offset:15872
	v_max3_f32 v152, v152, v107, v108
	s_waitcnt lgkmcnt(6)
	v_mfma_f32_32x32x16_bf16 v[66:81], v[2:5], v[216:219], v[66:81]
	v_max3_f32 v173, v173, v123, v124
	s_min_u32 s14, s97, 0x7c
	s_lshl_b32 s14, s14, 17
	s_add_i32 s14, s14, 0x60000
	buffer_load_dwordx4 v[224:227], v170, s[8:11], s14 offen
	s_waitcnt lgkmcnt(4)
	v_mfma_f32_32x32x16_bf16 v[66:81], v[6:9], v[220:223], v[66:81]
	v_max3_f32 v152, v152, v109, v110
	s_add_i32 s19, s36, 0xffff0000
	s_mov_b32 s14, s10
	s_mov_b32 s15, s11
	buffer_load_dwordx4 v[228:231], v171, s[12:15], s19 offen
	s_waitcnt lgkmcnt(2)
	v_mfma_f32_32x32x16_bf16 v[66:81], v[10:13], v[236:239], v[66:81]
	v_max3_f32 v173, v173, v125, v126
	buffer_load_dwordx4 v[232:235], v171, s[12:15], s36 offen
	s_waitcnt lgkmcnt(0)
	v_mfma_f32_32x32x16_bf16 v[66:81], v[14:17], v[198:201], v[66:81]
	v_max3_f32 v152, v152, v111, v112
	v_mfma_f32_4x4x4_16b_bf16 v[240:243], v[2:3], v[132:133], v[240:243]
	v_max3_f32 v173, v173, v127, v128
	v_mfma_f32_4x4x4_16b_bf16 v[244:247], v[4:5], v[132:133], v[244:247]
	v_mfma_f32_4x4x4_16b_bf16 v[240:243], v[6:7], v[132:133], v[240:243]
	v_max_f32 v152, v152, v113
	v_mfma_f32_4x4x4_16b_bf16 v[244:247], v[8:9], v[132:133], v[244:247]
	v_mfma_f32_4x4x4_16b_bf16 v[240:243], v[10:11], v[132:133], v[240:243]
	v_max_f32 v173, v173, v129
	v_mfma_f32_4x4x4_16b_bf16 v[244:247], v[12:13], v[132:133], v[244:247]
	v_mfma_f32_4x4x4_16b_bf16 v[240:243], v[14:15], v[132:133], v[240:243]
	v_max_f32 v173, v173, v152
	v_mfma_f32_4x4x4_16b_bf16 v[244:247], v[16:17], v[132:133], v[244:247]
	s_setprio 0
	s_barrier
	s_add_i32 s36, s36, 0x20000
	s_add_i32 s97, s97, 1
	s_cmpk_eq_i32 s97, 0x7e
	s_cbranch_scc1 .Lu3_exit_b1_2
	s_branch .Lu3_b1_0
.Lu3_exit_b1_0:
	s_mov_b32 s18, 0x2400
	s_mov_b32 s37, 0x4000
	s_mov_b32 s93, 0x0
	s_mov_b32 s94, 0x0
	s_mov_b32 s95, 0x8000
	s_mov_b32 s96, 0x4800
	s_branch .LBB0_290
.Lu3_rare_b1_0:
	s_mov_b32 s101, 0
	s_branch .LBB0_285
.Lu3_exit_b1_1:
	s_mov_b32 s18, 0x4800
	s_mov_b32 s37, 0x8000
	s_mov_b32 s93, 0x4000
	s_mov_b32 s94, 0x2400
	s_mov_b32 s95, 0x0
	s_mov_b32 s96, 0x0
	s_branch .LBB0_290
.Lu3_rare_b1_1:
	s_mov_b32 s101, 1
	s_branch .LBB0_285
.Lu3_exit_b1_2:
	s_mov_b32 s18, 0x0
	s_mov_b32 s37, 0x0
	s_mov_b32 s93, 0x8000
	s_mov_b32 s94, 0x4800
	s_mov_b32 s95, 0x4000
	s_mov_b32 s96, 0x2400
	s_branch .LBB0_290
.Lu3_rare_b1_2:
	s_mov_b32 s101, 2
	s_branch .LBB0_285

; __device__ __forceinline__ float softmax_shift(f32x16& p0, f32x16& p1, f32x16& negm, float pmax, bool first) {
;   asm volatile("s_nop 4" ::: "memory");
;   { auto rr = __builtin_amdgcn_permlane32_swap(__float_as_uint(pmax), __float_as_uint(pmax), false, false);
;     pmax = fmaxf(__uint_as_float(rr[0]), __uint_as_float(rr[1])); }
;   const float delta = first ? pmax : fmaxf(pmax, 0.f);
; #pragma unroll
;   for (int r = 0; r < 16; ++r) { p0[r] -= delta; p1[r] -= delta; negm[r] -= delta; }
;   return first ? 1.f : __builtin_amdgcn_exp2f(-delta);
; }
.LBB0_289:
	v_sub_f32_e32 v113, v113, v173
	v_sub_f32_e32 v112, v112, v173
	v_sub_f32_e32 v111, v111, v173
	v_sub_f32_e32 v110, v110, v173
	v_sub_f32_e32 v109, v109, v173
	v_sub_f32_e32 v108, v108, v173
	v_sub_f32_e32 v107, v107, v173
	v_sub_f32_e32 v106, v106, v173
	v_sub_f32_e32 v105, v105, v173
	v_sub_f32_e32 v104, v104, v173
	v_sub_f32_e32 v103, v103, v173
	v_sub_f32_e32 v102, v102, v173
	v_sub_f32_e32 v101, v101, v173
	v_sub_f32_e32 v100, v100, v173
	v_sub_f32_e32 v99, v99, v173
	v_sub_f32_e32 v98, v98, v173
	v_sub_f32_e32 v129, v129, v173
	v_sub_f32_e32 v128, v128, v173
	v_sub_f32_e32 v127, v127, v173
	v_sub_f32_e32 v126, v126, v173
	v_sub_f32_e32 v125, v125, v173
	v_sub_f32_e32 v124, v124, v173
	v_sub_f32_e32 v123, v123, v173
	v_sub_f32_e32 v122, v122, v173
	v_sub_f32_e32 v121, v121, v173
	v_sub_f32_e32 v120, v120, v173
	v_sub_f32_e32 v119, v119, v173
	v_sub_f32_e32 v118, v118, v173
	v_sub_f32_e32 v117, v117, v173
	v_sub_f32_e32 v116, v116, v173
	v_sub_f32_e32 v115, v115, v173
	v_sub_f32_e32 v114, v114, v173
	v_sub_f32_e32 v97, v97, v173
	v_sub_f32_e32 v96, v96, v173
	v_sub_f32_e32 v95, v95, v173
	v_sub_f32_e32 v94, v94, v173
	v_sub_f32_e32 v93, v93, v173
	v_sub_f32_e32 v92, v92, v173
	v_sub_f32_e32 v91, v91, v173
	v_sub_f32_e32 v90, v90, v173
	v_sub_f32_e32 v89, v89, v173
	v_sub_f32_e32 v88, v88, v173
	v_sub_f32_e32 v87, v87, v173
	v_sub_f32_e32 v86, v86, v173
	v_sub_f32_e32 v85, v85, v173
	v_sub_f32_e32 v84, v84, v173
	v_sub_f32_e32 v83, v83, v173
	v_sub_f32_e32 v82, v82, v173
	s_cmp_eq_u32 s101, 0
	s_cbranch_scc1 .LBB0_283
	s_cmp_eq_u32 s101, 1
	s_cbranch_scc1 .Lu3_join_b1_1
	s_branch .Lu3_join_b1_2

; __device__ __forceinline__ float softmax_rowmax(const f32x16& p0, const f32x16& p1) {
;   const float m0 = p1[0] + 0.0f; float a, b;
;   asm("v_max3_f32 %0, %1, %2, %3\n\tv_max3_f32 %0, %0, %4, %5\n\tv_max3_f32 %0, %0, %6, %7\n\tv_max3_f32 %0, %0, %8, %9\n\t"
;       "v_max3_f32 %0, %0, %10, %11\n\tv_max3_f32 %0, %0, %12, %13\n\tv_max3_f32 %0, %0, %14, %15\n\tv_max3_f32 %0, %0, %16, %17"
;       : "=&v"(a) : "v"(m0), "v"(p0[0]), "v"(p0[1]), "v"(p0[2]), "v"(p0[3]), "v"(p0[4]), "v"(p0[5]), "v"(p0[6]), "v"(p0[7]), "v"(p0[8]), "v"(p0[9]), "v"(p0[10]), "v"(p0[11]), "v"(p0[12]), "v"(p0[13]), "v"(p0[14]), "v"(p0[15]));
;   asm("v_max3_f32 %0, %1, %2, %3\n\tv_max3_f32 %0, %0, %4, %5\n\tv_max3_f32 %0, %0, %6, %7\n\tv_max3_f32 %0, %0, %8, %9\n\t"
;       "v_max3_f32 %0, %0, %10, %11\n\tv_max3_f32 %0, %0, %12, %13\n\tv_max3_f32 %0, %0, %14, %15\n\tv_max_f32 %0, %0, %16"
;       : "=&v"(b) : "v"(a), "v"(p1[1]), "v"(p1[2]), "v"(p1[3]), "v"(p1[4]), "v"(p1[5]), "v"(p1[6]), "v"(p1[7]), "v"(p1[8]), "v"(p1[9]), "v"(p1[10]), "v"(p1[11]), "v"(p1[12]), "v"(p1[13]), "v"(p1[14]), "v"(p1[15]));
;   return b;
; }
; __device__ __forceinline__ float softmax_shift(f32x16& p0, f32x16& p1, f32x16& negm, float pmax, bool first) {
;   asm volatile("s_nop 4" ::: "memory");
;   { auto rr = __builtin_amdgcn_permlane32_swap(__float_as_uint(pmax), __float_as_uint(pmax), false, false);
;     pmax = fmaxf(__uint_as_float(rr[0]), __uint_as_float(rr[1])); }
;   const float delta = first ? pmax : fmaxf(pmax, 0.f);
; #pragma unroll
;   for (int r = 0; r < 16; ++r) { p0[r] -= delta; p1[r] -= delta; negm[r] -= delta; }
;   return first ? 1.f : __builtin_amdgcn_exp2f(-delta);
; }
; __device__ __forceinline__ void softmax_exp_pack(f32x16& p0, f32x16& p1, bf16x8& pa0, bf16x8& pa1, bf16x8& pa2, bf16x8& pa3) {
; #pragma unroll
;   for (int r = 0; r < 16; ++r) { p0[r] = __builtin_amdgcn_exp2f(p0[r]); p1[r] = __builtin_amdgcn_exp2f(p1[r]); }
;     ...
;   ATT_PK4(p0, 0, pa0); ATT_PK4(p0, 8, pa1); ATT_PK4(p1, 0, pa2); ATT_PK4(p1, 8, pa3);
;     ...
; }
;     ...
;   for (int t = 0; t + 1 < NT; ++t) {
;     if constexpr (ABL & 1) { u32x4 w0 = {cvtpk(p0[0], p0[1]), cvtpk(p0[2], p0[3]), cvtpk(p0[4], p0[5]), cvtpk(p0[6], p0[7])}, w1 = {cvtpk(p0[8], p0[9]), cvtpk(p0[10], p0[11]), cvtpk(p0[12], p0[13]), cvtpk(p0[14], p0[15])};
.LBB0_296:
	v_mul_u32_u24_e32 v2, 0x90, v62
	v_add3_u32 v78, 0, v184, v2
	ds_read_b128 v[2:5], v78 offset:49152
	v_mad_u32_u24 v167, v62, s82, 0
	v_add_u32_e32 v173, v167, v184
	ds_read_b128 v[34:37], v173 offset:53760
	ds_read_b128 v[66:69], v78 offset:49184
	ds_read_b128 v[70:73], v78 offset:49216
	v_and_b32_e32 v63, 63, v63
	s_mov_b32 s90, 1
	s_waitcnt lgkmcnt(3)
	v_mfma_f32_32x32x16_bf16 v[2:17], v[2:5], v[136:139], 0
	s_waitcnt lgkmcnt(2)
	v_mfma_f32_32x32x16_bf16 v[34:49], v[34:37], v[136:139], 0
	s_waitcnt lgkmcnt(1)
	v_mfma_f32_32x32x16_bf16 v[2:17], v[66:69], v[140:143], v[2:17]
	ds_read_b128 v[66:69], v78 offset:53792
	ds_read_b128 v[74:77], v78 offset:49248
	s_waitcnt lgkmcnt(1)
	v_mfma_f32_32x32x16_bf16 v[34:49], v[66:69], v[140:143], v[34:49]
	v_mfma_f32_32x32x16_bf16 v[2:17], v[70:73], v[144:147], v[2:17]
	ds_read_b128 v[66:69], v78 offset:53824
	ds_read_b128 v[70:73], v78 offset:53856
	s_waitcnt lgkmcnt(1)
	v_mfma_f32_32x32x16_bf16 v[34:49], v[66:69], v[144:147], v[34:49]
	v_lshlrev_b32_e32 v67, 3, v63
	v_lshlrev_b32_e32 v69, 4, v63
	v_add_u32_e32 v66, 0xc000, v170
	v_and_b32_e32 v68, 24, v67
	v_and_b32_e32 v69, 0xc0, v69
	v_and_b32_e32 v67, 0x100, v67
	v_mfma_f32_32x32x16_bf16 v[2:17], v[74:77], v[148:151], v[2:17]
	v_lshlrev_b32_e32 v74, 1, v63
	v_and_b32_e32 v74, 32, v74
	s_waitcnt lgkmcnt(0)
	v_mfma_f32_32x32x16_bf16 v[34:49], v[70:73], v[148:151], v[34:49]
	s_barrier
	v_cmp_gt_u32_e64 s[4:5], 32, v63
	v_lshl_add_u32 v166, v62, 2, s6
	s_nop 9
	v_add_f32_e32 v62, 0, v34
	v_max3_f32 v63, v62, v2, v3
	v_max3_f32 v63, v63, v4, v5
	v_max3_f32 v63, v63, v6, v7
	v_max3_f32 v63, v63, v8, v9
	v_max3_f32 v63, v63, v10, v11
	v_max3_f32 v63, v63, v12, v13
	v_max3_f32 v63, v63, v14, v15
	v_max3_f32 v63, v63, v16, v17
	s_nop 4
	v_add3_u32 v68, 0, v68, v69
	v_max3_f32 v62, v63, v35, v36
	v_max3_f32 v62, v62, v37, v38
	v_max3_f32 v62, v62, v39, v40
	v_max3_f32 v62, v62, v41, v42
	v_max3_f32 v62, v62, v43, v44
	v_max3_f32 v62, v62, v45, v46
	v_max3_f32 v62, v62, v47, v48
	v_max_f32 v62, v62, v49
	v_add3_u32 v131, v68, v74, v67
	v_mov_b32_e32 v63, v62
	s_nop 1
	v_permlane32_swap_b32_e32 v62, v63
	v_max_f32_e32 v63, v63, v63
	v_max_f32_e32 v62, v62, v62
	v_max_f32_e32 v62, v62, v63
	v_sub_f32_e32 v2, v2, v62
	v_sub_f32_e32 v34, v34, v62
	v_sub_f32_e32 v3, v3, v62
	v_sub_f32_e32 v35, v35, v62
	v_sub_f32_e32 v4, v4, v62
	v_sub_f32_e32 v36, v36, v62
	v_sub_f32_e32 v5, v5, v62
	v_sub_f32_e32 v37, v37, v62
	v_sub_f32_e32 v6, v6, v62
	v_sub_f32_e32 v38, v38, v62
	v_sub_f32_e32 v7, v7, v62
	v_sub_f32_e32 v39, v39, v62
	v_sub_f32_e32 v8, v8, v62
	v_sub_f32_e32 v40, v40, v62
	v_sub_f32_e32 v9, v9, v62
	v_sub_f32_e32 v41, v41, v62
	v_sub_f32_e32 v10, v10, v62
	v_sub_f32_e32 v42, v42, v62
	v_sub_f32_e32 v11, v11, v62
	v_sub_f32_e32 v43, v43, v62
	v_sub_f32_e32 v12, v12, v62
	v_sub_f32_e32 v44, v44, v62
	v_sub_f32_e32 v13, v13, v62
	v_sub_f32_e32 v45, v45, v62
	v_sub_f32_e32 v14, v14, v62
	v_sub_f32_e32 v46, v46, v62
	v_sub_f32_e32 v15, v15, v62
	v_sub_f32_e32 v47, v47, v62
	v_sub_f32_e32 v16, v16, v62
	v_sub_f32_e32 v48, v48, v62
	v_sub_f32_e32 v17, v17, v62
	v_sub_f32_e32 v49, v49, v62
	v_exp_f32_e32 v2, v2
	v_exp_f32_e32 v34, v34
	v_exp_f32_e32 v3, v3
	v_exp_f32_e32 v35, v35
	v_exp_f32_e32 v4, v4
	v_exp_f32_e32 v36, v36
	v_exp_f32_e32 v5, v5
	v_exp_f32_e32 v37, v37
	v_exp_f32_e32 v6, v6
	v_exp_f32_e32 v38, v38
	v_exp_f32_e32 v7, v7
	v_exp_f32_e32 v39, v39
	v_exp_f32_e32 v8, v8
	v_exp_f32_e32 v40, v40
	v_exp_f32_e32 v9, v9
	v_exp_f32_e32 v41, v41
	v_exp_f32_e32 v10, v10
	v_exp_f32_e32 v42, v42
	v_exp_f32_e32 v11, v11
	v_exp_f32_e32 v43, v43
	v_exp_f32_e32 v12, v12
	v_exp_f32_e32 v44, v44
	v_exp_f32_e32 v13, v13
	v_exp_f32_e32 v45, v45
	v_exp_f32_e32 v14, v14
	v_exp_f32_e32 v46, v46
	v_exp_f32_e32 v15, v15
	v_exp_f32_e32 v47, v47
	v_exp_f32_e32 v16, v16
	v_exp_f32_e32 v48, v48
	v_exp_f32_e32 v17, v17
	v_exp_f32_e32 v49, v49
	v_sub_f32_e32 v82, 0, v62
	v_mov_b32_e32 v83, v82
	v_mov_b32_e32 v84, v82
	v_mov_b32_e32 v85, v82
	v_mov_b32_e32 v86, v82
	v_mov_b32_e32 v87, v82
	v_mov_b32_e32 v88, v82
	v_mov_b32_e32 v89, v82
	v_mov_b32_e32 v90, v82
	v_mov_b32_e32 v91, v82
	v_mov_b32_e32 v92, v82
	v_mov_b32_e32 v93, v82
	v_mov_b32_e32 v94, v82
	v_mov_b32_e32 v95, v82
	v_mov_b32_e32 v96, v82
	v_mov_b32_e32 v97, v82
	v_cvt_pk_bf16_f32 v98, v2, v3
	v_cvt_pk_bf16_f32 v99, v4, v5
	v_cvt_pk_bf16_f32 v100, v6, v7
	v_cvt_pk_bf16_f32 v101, v8, v9
	v_cvt_pk_bf16_f32 v102, v10, v11
	v_cvt_pk_bf16_f32 v103, v12, v13
	v_cvt_pk_bf16_f32 v104, v14, v15
	v_cvt_pk_bf16_f32 v105, v16, v17
	v_cvt_pk_bf16_f32 v106, v34, v35
	v_cvt_pk_bf16_f32 v107, v36, v37
	v_cvt_pk_bf16_f32 v108, v38, v39
	v_cvt_pk_bf16_f32 v109, v40, v41
	v_cvt_pk_bf16_f32 v110, v42, v43
	v_cvt_pk_bf16_f32 v111, v44, v45
	v_cvt_pk_bf16_f32 v112, v46, v47
	v_cvt_pk_bf16_f32 v113, v48, v49
	s_waitcnt vmcnt(1)
	ds_write_b128 v66, v[58:61] offset:18432
	ds_write_b128 v64, v[50:53] offset:16384
	s_waitcnt vmcnt(0)
	ds_write_b128 v65, v[54:57] offset:16384
	ds_read_b64_tr_b16 v[2:3], v131
	ds_read_b64_tr_b16 v[4:5], v131 offset:2048
	ds_read_b64_tr_b16 v[6:7], v131 offset:4096
	ds_read_b64_tr_b16 v[8:9], v131 offset:6144
	ds_read_b64_tr_b16 v[10:11], v131 offset:8192
	ds_read_b64_tr_b16 v[12:13], v131 offset:10240
	ds_read_b64_tr_b16 v[14:15], v131 offset:12288
	ds_read_b64_tr_b16 v[16:17], v131 offset:14336
	s_waitcnt lgkmcnt(8)
	s_barrier
; #define ATT_SBAR() __builtin_amdgcn_sched_barrier(0)
; __device__ __forceinline__ float softmax_rowmax(const f32x16& p0, const f32x16& p1) {
;   const float m0 = p1[0] + 0.0f; float a, b;
;   asm("v_max3_f32 %0, %1, %2, %3\n\tv_max3_f32 %0, %0, %4, %5\n\tv_max3_f32 %0, %0, %6, %7\n\tv_max3_f32 %0, %0, %8, %9\n\t"
;       "v_max3_f32 %0, %0, %10, %11\n\tv_max3_f32 %0, %0, %12, %13\n\tv_max3_f32 %0, %0, %14, %15\n\tv_max3_f32 %0, %0, %16, %17"
;       : "=&v"(a) : "v"(m0), "v"(p0[0]), "v"(p0[1]), "v"(p0[2]), "v"(p0[3]), "v"(p0[4]), "v"(p0[5]), "v"(p0[6]), "v"(p0[7]), "v"(p0[8]), "v"(p0[9]), "v"(p0[10]), "v"(p0[11]), "v"(p0[12]), "v"(p0[13]), "v"(p0[14]), "v"(p0[15]));
;   asm("v_max3_f32 %0, %1, %2, %3\n\tv_max3_f32 %0, %0, %4, %5\n\tv_max3_f32 %0, %0, %6, %7\n\tv_max3_f32 %0, %0, %8, %9\n\t"
;       "v_max3_f32 %0, %0, %10, %11\n\tv_max3_f32 %0, %0, %12, %13\n\tv_max3_f32 %0, %0, %14, %15\n\tv_max_f32 %0, %0, %16"
;       : "=&v"(b) : "v"(a), "v"(p1[1]), "v"(p1[2]), "v"(p1[3]), "v"(p1[4]), "v"(p1[5]), "v"(p1[6]), "v"(p1[7]), "v"(p1[8]), "v"(p1[9]), "v"(p1[10]), "v"(p1[11]), "v"(p1[12]), "v"(p1[13]), "v"(p1[14]), "v"(p1[15]));
;   return b;
;     ...
;   for (int t = 0; t + 1 < NT; ++t) {
;     if constexpr (ABL & 1) { u32x4 w0 = {cvtpk(p0[0], p0[1]), cvtpk(p0[2], p0[3]), cvtpk(p0[4], p0[5]), cvtpk(p0[6], p0[7])}, w1 = {cvtpk(p0[8], p0[9]), cvtpk(p0[10], p0[11]), cvtpk(p0[12], p0[13]), cvtpk(p0[14], p0[15])};
;         u32x4 w2 = {cvtpk(p1[0], p1[1]), cvtpk(p1[2], p1[3]), cvtpk(p1[4], p1[5]), cvtpk(p1[6], p1[7])}, w3 = {cvtpk(p1[8], p1[9]), cvtpk(p1[10], p1[11]), cvtpk(p1[12], p1[13]), cvtpk(p1[14], p1[15])};
;         pa0 = *reinterpret_cast<bf16x8*>(&w0); pa1 = *reinterpret_cast<bf16x8*>(&w1); pa2 = *reinterpret_cast<bf16x8*>(&w2); pa3 = *reinterpret_cast<bf16x8*>(&w3); }
;     else { ATT_SOFTMAX(t == 0); }
;     if constexpr (!(ABL & 4)) { ATT_WRITE_K(k2); ATT_WRITE_V(v1); }
;     ATT_SBAR();
; #pragma unroll
;     for (int ks = 0; ks < 4; ++ks) ATT_VPAIR(va, v0, 0, ks);
;     asm volatile("s_waitcnt lgkmcnt(8)" ::: "memory"); ATT_BAR();
;     ATT_XSECTION(true);
;     if constexpr (!(ABL & 4)) { const int tk = (t + 3 < NT) ? t + 3 : NT - 1, tv = (t + 2 < NT) ? t + 2 : NT - 1; ATT_LOAD_K(tk); ATT_LOAD_V(tv); }
;     ATT_BAR();
;     { const int tk_ = k0; k0 = k1; k1 = k2; k2 = tk_; const int tv_ = v0; v0 = v1; v1 = v2; v2 = tv_; }
;   }
	s_setprio 2
	s_waitcnt lgkmcnt(6)
	v_mfma_f32_32x32x16_bf16 v[66:81], v[98:101], v[2:5], 0
	ds_read_b64_tr_b16 v[34:35], v131 offset:512
	ds_read_b64_tr_b16 v[36:37], v131 offset:2560
	s_waitcnt lgkmcnt(6)
	v_mfma_f32_32x32x16_bf16 v[66:81], v[102:105], v[6:9], v[66:81]
	ds_read_b64_tr_b16 v[2:3], v131 offset:4608
	ds_read_b64_tr_b16 v[4:5], v131 offset:6656
	s_waitcnt lgkmcnt(6)
	v_mfma_f32_32x32x16_bf16 v[66:81], v[106:109], v[10:13], v[66:81]
	ds_read_b64_tr_b16 v[6:7], v131 offset:8704
	ds_read_b64_tr_b16 v[8:9], v131 offset:10752
	s_waitcnt lgkmcnt(6)
	v_mfma_f32_32x32x16_bf16 v[66:81], v[110:113], v[14:17], v[66:81]
	ds_read_b64_tr_b16 v[10:11], v131 offset:12800
	ds_read_b64_tr_b16 v[12:13], v131 offset:14848
	s_waitcnt lgkmcnt(6)
	v_mfma_f32_32x32x16_bf16 v[50:65], v[98:101], v[34:37], 0
	ds_read_b64_tr_b16 v[14:15], v131 offset:1024
	ds_read_b64_tr_b16 v[16:17], v131 offset:3072
	s_waitcnt lgkmcnt(6)
	v_mfma_f32_32x32x16_bf16 v[50:65], v[102:105], v[2:5], v[50:65]
	ds_read_b64_tr_b16 v[114:115], v131 offset:5120
	ds_read_b64_tr_b16 v[116:117], v131 offset:7168
	s_waitcnt lgkmcnt(6)
	v_mfma_f32_32x32x16_bf16 v[50:65], v[106:109], v[6:9], v[50:65]
	ds_read_b64_tr_b16 v[2:3], v131 offset:9216
	ds_read_b64_tr_b16 v[4:5], v131 offset:11264
	s_waitcnt lgkmcnt(6)
	v_mfma_f32_32x32x16_bf16 v[50:65], v[110:113], v[10:13], v[50:65]
	ds_read_b64_tr_b16 v[6:7], v131 offset:13312
	ds_read_b64_tr_b16 v[8:9], v131 offset:15360
	s_waitcnt lgkmcnt(6)
	v_mfma_f32_32x32x16_bf16 v[34:49], v[98:101], v[14:17], 0
	ds_read_b64_tr_b16 v[10:11], v131 offset:1536
	ds_read_b64_tr_b16 v[12:13], v131 offset:3584
	s_waitcnt lgkmcnt(6)
	v_mfma_f32_32x32x16_bf16 v[34:49], v[102:105], v[114:117], v[34:49]
	ds_read_b64_tr_b16 v[118:119], v131 offset:5632
	ds_read_b64_tr_b16 v[120:121], v131 offset:7680
	s_waitcnt lgkmcnt(6)
	v_mfma_f32_32x32x16_bf16 v[34:49], v[106:109], v[2:5], v[34:49]
	ds_read_b64_tr_b16 v[114:115], v131 offset:9728
	ds_read_b64_tr_b16 v[116:117], v131 offset:11776
	s_waitcnt lgkmcnt(6)
	v_mfma_f32_32x32x16_bf16 v[34:49], v[110:113], v[6:9], v[34:49]
	ds_read_b64_tr_b16 v[122:123], v131 offset:13824
	ds_read_b64_tr_b16 v[124:125], v131 offset:15872
	s_waitcnt lgkmcnt(6)
	v_mfma_f32_32x32x16_bf16 v[2:17], v[98:101], v[10:13], 0
	ds_read_b128 v[126:129], v173 offset:58368
	s_waitcnt lgkmcnt(5)
	v_mfma_f32_32x32x16_bf16 v[2:17], v[102:105], v[118:121], v[2:17]
	ds_read_b128 v[152:155], v173 offset:62976
	s_waitcnt lgkmcnt(4)
	v_mfma_f32_32x32x16_bf16 v[2:17], v[106:109], v[114:117], v[2:17]
	ds_read_b128 v[156:159], v173 offset:58400
	s_waitcnt lgkmcnt(3)
	v_mfma_f32_32x32x16_bf16 v[2:17], v[110:113], v[122:125], v[2:17]
	ds_read_b128 v[160:163], v173 offset:63008
	v_mfma_f32_4x4x4_16b_bf16 v[240:243], v[98:99], v[132:133], 0
	ds_read_b128 v[174:177], v173 offset:58432
	v_mfma_f32_4x4x4_16b_bf16 v[244:247], v[100:101], v[132:133], 0
	v_mfma_f32_4x4x4_16b_bf16 v[240:243], v[102:103], v[132:133], v[240:243]
	ds_read_b128 v[178:181], v173 offset:63040
	v_mfma_f32_4x4x4_16b_bf16 v[244:247], v[104:105], v[132:133], v[244:247]
	v_mfma_f32_4x4x4_16b_bf16 v[240:243], v[106:107], v[132:133], v[240:243]
	ds_read_b128 v[186:189], v173 offset:58464
	v_mfma_f32_4x4x4_16b_bf16 v[244:247], v[108:109], v[132:133], v[244:247]
	v_mfma_f32_4x4x4_16b_bf16 v[240:243], v[110:111], v[132:133], v[240:243]
	ds_read_b128 v[190:193], v173 offset:63072
	v_mfma_f32_4x4x4_16b_bf16 v[244:247], v[112:113], v[132:133], v[244:247]
	s_waitcnt lgkmcnt(7)
	v_mfma_f32_32x32x16_bf16 v[98:113], v[126:129], v[136:139], v[82:97]
	v_mov_b64_e32 v[128:129], v[96:97]
	v_mov_b64_e32 v[126:127], v[94:95]
	v_mov_b64_e32 v[124:125], v[92:93]
	v_mov_b64_e32 v[122:123], v[90:91]
	v_mov_b64_e32 v[120:121], v[88:89]
	v_mov_b64_e32 v[118:119], v[86:87]
	v_mov_b64_e32 v[116:117], v[84:85]
	v_mov_b64_e32 v[114:115], v[82:83]
	s_waitcnt lgkmcnt(6)
	s_nop 0
	v_mfma_f32_32x32x16_bf16 v[114:129], v[152:155], v[136:139], v[114:129]
	s_waitcnt lgkmcnt(5)
	v_mfma_f32_32x32x16_bf16 v[98:113], v[156:159], v[140:143], v[98:113]
	s_waitcnt lgkmcnt(4)
	v_mfma_f32_32x32x16_bf16 v[114:129], v[160:163], v[140:143], v[114:129]
	s_waitcnt lgkmcnt(3)
	v_mfma_f32_32x32x16_bf16 v[98:113], v[174:177], v[144:147], v[98:113]
	s_waitcnt lgkmcnt(2)
	v_mfma_f32_32x32x16_bf16 v[114:129], v[178:181], v[144:147], v[114:129]
	s_waitcnt lgkmcnt(1)
	v_mfma_f32_32x32x16_bf16 v[98:113], v[186:189], v[148:151], v[98:113]
	s_waitcnt lgkmcnt(0)
	v_mfma_f32_32x32x16_bf16 v[114:129], v[190:193], v[148:151], v[114:129]
	s_setprio 0
	buffer_load_dwordx4 v[224:227], v171, s[8:11], s85 offen
	buffer_load_dwordx4 v[228:231], v172, s[12:15], s83 offen
	buffer_load_dwordx4 v[232:235], v172, s[12:15], s86 offen
	s_barrier
	s_mov_b32 s50, 0x8000
	s_movk_i32 s15, 0x4000
	s_movk_i32 s51, 0x2400
	s_mov_b32 s49, 0
	s_movk_i32 s14, 0x4800
	s_mov_b32 s36, 0x70000
	s_mov_b32 s48, 0
	s_nop 0
	v_add_f32_e32 v174, 0, v114
	v_max3_f32 v175, v174, v98, v99
	v_max3_f32 v175, v175, v100, v101
	v_max3_f32 v175, v175, v102, v103
	v_max3_f32 v175, v175, v104, v105
	v_max3_f32 v175, v175, v106, v107
	v_max3_f32 v175, v175, v108, v109
	v_max3_f32 v175, v175, v110, v111
	v_max3_f32 v175, v175, v112, v113
	v_max3_f32 v174, v175, v115, v116
	v_max3_f32 v174, v174, v117, v118
	v_max3_f32 v174, v174, v119, v120
	v_max3_f32 v174, v174, v121, v122
	v_max3_f32 v174, v174, v123, v124
	v_max3_f32 v174, v174, v125, v126
	v_max3_f32 v174, v174, v127, v128
	v_max_f32 v174, v174, v129
	v_add_u32_e32 v248, 0x8000, v170
	v_add_u32_e32 v249, 0x8000, v173
.LBB0_297:
.Lu3_b2_0:
	v_cmp_ge_f32_e32 vcc, s60, v174
	s_cmp_eq_u64 vcc, exec
	s_cbranch_scc0 .Lu3_rare_b2_0
; #define ATT_SBAR() __builtin_amdgcn_sched_barrier(0)
; #define ATT_PK4(P, BASE, OUT) do { u32x4 w = {cvtpk(P[BASE + 0], P[BASE + 1]), cvtpk(P[BASE + 2], P[BASE + 3]), cvtpk(P[BASE + 4], P[BASE + 5]), cvtpk(P[BASE + 6], P[BASE + 7])}; \
;     OUT = *reinterpret_cast<bf16x8*>(&w); } while (0)
; #define ATT_WRITE_K(so) do { *(bf16x8*)(K_lds + (so) + kswz<DQK>(kr, kc * 2)) = sk0; if constexpr (DQK == 128) *(bf16x8*)(K_lds + (so) + kswz<DQK>(32 + kr, kc * 2)) = sk1; } while (0)
; #define ATT_WRITE_V(so) do { *(bf16x8*)(V_lds + (so) + vst0) = sv0; *(bf16x8*)(V_lds + (so) + vst1) = sv1; } while (0)
; #define ATT_BAR() do { ATT_SBAR(); asm volatile("s_barrier" ::: "memory"); ATT_SBAR(); } while (0)
; #define ATT_VPAIR(buf, so, blk, ks) do { if constexpr (!(ABL & 8) && !(ABL & 32)) { buf[2 * (ks)] = vtr(vq0 + (so) + v_rd_off(blk, ks, 0)); buf[2 * (ks) + 1] = vtr(vq0 + (so) + v_rd_off(blk, ks, 1)); } } while (0)
; __device__ __forceinline__ void softmax_exp_pack(f32x16& p0, f32x16& p1, bf16x8& pa0, bf16x8& pa1, bf16x8& pa2, bf16x8& pa3) {
; #pragma unroll
;   for (int r = 0; r < 16; ++r) { p0[r] = __builtin_amdgcn_exp2f(p0[r]); p1[r] = __builtin_amdgcn_exp2f(p1[r]); }
;     ...
;   ATT_PK4(p0, 0, pa0); ATT_PK4(p0, 8, pa1); ATT_PK4(p1, 0, pa2); ATT_PK4(p1, 8, pa3);
;     ...
;     if constexpr (!(ABL & 4)) { ATT_WRITE_K(k2); ATT_WRITE_V(v1); }
;     ATT_SBAR();
; #pragma unroll
;     for (int ks = 0; ks < 4; ++ks) ATT_VPAIR(va, v0, 0, ks);
;     asm volatile("s_waitcnt lgkmcnt(8)" ::: "memory"); ATT_BAR();
.LBB0_298:
	v_exp_f32_e32 v98, v98
	v_exp_f32_e32 v114, v114
	v_exp_f32_e32 v99, v99
	v_exp_f32_e32 v115, v115
	v_exp_f32_e32 v100, v100
	v_exp_f32_e32 v101, v101
	v_exp_f32_e32 v102, v102
	v_exp_f32_e32 v103, v103
	v_exp_f32_e32 v106, v106
	v_exp_f32_e32 v107, v107
	v_exp_f32_e32 v116, v116
	v_exp_f32_e32 v117, v117
	v_exp_f32_e32 v118, v118
	v_exp_f32_e32 v119, v119
	v_exp_f32_e32 v104, v104
	v_exp_f32_e32 v120, v120
	v_exp_f32_e32 v105, v105
	v_exp_f32_e32 v121, v121
	v_exp_f32_e32 v122, v122
	v_exp_f32_e32 v123, v123
	v_exp_f32_e32 v108, v108
	v_exp_f32_e32 v124, v124
	v_exp_f32_e32 v109, v109
	v_exp_f32_e32 v125, v125
	v_exp_f32_e32 v110, v110
	v_exp_f32_e32 v126, v126
	v_exp_f32_e32 v111, v111
	v_exp_f32_e32 v127, v127
	v_exp_f32_e32 v112, v112
	v_exp_f32_e32 v128, v128
	v_exp_f32_e32 v113, v113
	v_exp_f32_e32 v129, v129
	v_cvt_pk_bf16_f32 v18, v98, v99
	v_cvt_pk_bf16_f32 v19, v100, v101
	v_cvt_pk_bf16_f32 v20, v102, v103
	v_cvt_pk_bf16_f32 v22, v106, v107
	v_cvt_pk_bf16_f32 v26, v114, v115
	v_cvt_pk_bf16_f32 v21, v104, v105
	v_cvt_pk_bf16_f32 v23, v108, v109
	v_cvt_pk_bf16_f32 v24, v110, v111
	v_cvt_pk_bf16_f32 v25, v112, v113
	v_cvt_pk_bf16_f32 v27, v116, v117
	v_cvt_pk_bf16_f32 v28, v118, v119
	v_cvt_pk_bf16_f32 v29, v120, v121
	v_cvt_pk_bf16_f32 v30, v122, v123
	v_cvt_pk_bf16_f32 v31, v124, v125
	v_cvt_pk_bf16_f32 v32, v126, v127
	v_cvt_pk_bf16_f32 v33, v128, v129
	s_waitcnt vmcnt(0)
	ds_write_b128 v248, v[224:227] offset:16384
	ds_write_b128 v168, v[228:231] offset:32768
	ds_write_b128 v169, v[232:235] offset:32768
	ds_read_b128 v[152:155], v249 offset:34816
	ds_read_b128 v[156:159], v249 offset:39424
	ds_read_b128 v[160:163], v249 offset:34848
	ds_read_b128 v[176:179], v249 offset:39456
	s_waitcnt lgkmcnt(4)
	s_barrier
; #define ATT_SBAR() __builtin_amdgcn_sched_barrier(0)
; __device__ __forceinline__ float softmax_rowmax(const f32x16& p0, const f32x16& p1) {
;   const float m0 = p1[0] + 0.0f; float a, b;
;   asm("v_max3_f32 %0, %1, %2, %3\n\tv_max3_f32 %0, %0, %4, %5\n\tv_max3_f32 %0, %0, %6, %7\n\tv_max3_f32 %0, %0, %8, %9\n\t"
;       "v_max3_f32 %0, %0, %10, %11\n\tv_max3_f32 %0, %0, %12, %13\n\tv_max3_f32 %0, %0, %14, %15\n\tv_max3_f32 %0, %0, %16, %17"
;       : "=&v"(a) : "v"(m0), "v"(p0[0]), "v"(p0[1]), "v"(p0[2]), "v"(p0[3]), "v"(p0[4]), "v"(p0[5]), "v"(p0[6]), "v"(p0[7]), "v"(p0[8]), "v"(p0[9]), "v"(p0[10]), "v"(p0[11]), "v"(p0[12]), "v"(p0[13]), "v"(p0[14]), "v"(p0[15]));
;   asm("v_max3_f32 %0, %1, %2, %3\n\tv_max3_f32 %0, %0, %4, %5\n\tv_max3_f32 %0, %0, %6, %7\n\tv_max3_f32 %0, %0, %8, %9\n\t"
;       "v_max3_f32 %0, %0, %10, %11\n\tv_max3_f32 %0, %0, %12, %13\n\tv_max3_f32 %0, %0, %14, %15\n\tv_max_f32 %0, %0, %16"
;       : "=&v"(b) : "v"(a), "v"(p1[1]), "v"(p1[2]), "v"(p1[3]), "v"(p1[4]), "v"(p1[5]), "v"(p1[6]), "v"(p1[7]), "v"(p1[8]), "v"(p1[9]), "v"(p1[10]), "v"(p1[11]), "v"(p1[12]), "v"(p1[13]), "v"(p1[14]), "v"(p1[15]));
;   return b;
;     ...
;   for (int t = 0; t + 1 < NT; ++t) {
;     if constexpr (ABL & 1) { u32x4 w0 = {cvtpk(p0[0], p0[1]), cvtpk(p0[2], p0[3]), cvtpk(p0[4], p0[5]), cvtpk(p0[6], p0[7])}, w1 = {cvtpk(p0[8], p0[9]), cvtpk(p0[10], p0[11]), cvtpk(p0[12], p0[13]), cvtpk(p0[14], p0[15])};
;         u32x4 w2 = {cvtpk(p1[0], p1[1]), cvtpk(p1[2], p1[3]), cvtpk(p1[4], p1[5]), cvtpk(p1[6], p1[7])}, w3 = {cvtpk(p1[8], p1[9]), cvtpk(p1[10], p1[11]), cvtpk(p1[12], p1[13]), cvtpk(p1[14], p1[15])};
;         pa0 = *reinterpret_cast<bf16x8*>(&w0); pa1 = *reinterpret_cast<bf16x8*>(&w1); pa2 = *reinterpret_cast<bf16x8*>(&w2); pa3 = *reinterpret_cast<bf16x8*>(&w3); }
;     else { ATT_SOFTMAX(t == 0); }
;     if constexpr (!(ABL & 4)) { ATT_WRITE_K(k2); ATT_WRITE_V(v1); }
;     ATT_SBAR();
; #pragma unroll
;     for (int ks = 0; ks < 4; ++ks) ATT_VPAIR(va, v0, 0, ks);
;     asm volatile("s_waitcnt lgkmcnt(8)" ::: "memory"); ATT_BAR();
;     ATT_XSECTION(true);
;     if constexpr (!(ABL & 4)) { const int tk = (t + 3 < NT) ? t + 3 : NT - 1, tv = (t + 2 < NT) ? t + 2 : NT - 1; ATT_LOAD_K(tk); ATT_LOAD_V(tv); }
;     ATT_BAR();
;     { const int tk_ = k0; k0 = k1; k1 = k2; k2 = tk_; const int tv_ = v0; v0 = v1; v1 = v2; v2 = tv_; }
	s_setprio 2
	s_waitcnt lgkmcnt(3)
	v_mfma_f32_32x32x16_bf16 v[98:113], v[152:155], v[136:139], v[82:97]
	ds_read_b128 v[180:183], v249 offset:34880
	s_waitcnt lgkmcnt(3)
	v_mfma_f32_32x32x16_bf16 v[114:129], v[156:159], v[136:139], v[82:97]
	ds_read_b128 v[186:189], v249 offset:39488
	s_waitcnt lgkmcnt(3)
	v_mfma_f32_32x32x16_bf16 v[98:113], v[160:163], v[140:143], v[98:113]
	ds_read_b128 v[190:193], v249 offset:34912
	ds_read_b64_tr_b16 v[198:199], v131 offset:16384
	ds_read_b64_tr_b16 v[200:201], v131 offset:18432
	s_waitcnt lgkmcnt(5)
	v_mfma_f32_32x32x16_bf16 v[114:129], v[176:179], v[140:143], v[114:129]
	ds_read_b128 v[194:197], v249 offset:39520
	ds_read_b64_tr_b16 v[212:213], v131 offset:20480
	ds_read_b64_tr_b16 v[214:215], v131 offset:22528
	s_waitcnt lgkmcnt(7)
	v_mfma_f32_32x32x16_bf16 v[98:113], v[180:183], v[144:147], v[98:113]
	ds_read_b64_tr_b16 v[216:217], v131 offset:24576
	ds_read_b64_tr_b16 v[218:219], v131 offset:26624
	s_waitcnt lgkmcnt(8)
	v_mfma_f32_32x32x16_bf16 v[114:129], v[186:189], v[144:147], v[114:129]
	ds_read_b64_tr_b16 v[220:221], v131 offset:28672
	ds_read_b64_tr_b16 v[222:223], v131 offset:30720
	s_waitcnt lgkmcnt(9)
	v_mfma_f32_32x32x16_bf16 v[98:113], v[190:193], v[148:151], v[98:113]
	s_waitcnt lgkmcnt(6)
	v_mfma_f32_32x32x16_bf16 v[114:129], v[194:197], v[148:151], v[114:129]
	v_mfma_f32_32x32x16_bf16 v[66:81], v[18:21], v[198:201], v[66:81]
	ds_read_b64_tr_b16 v[236:237], v131 offset:16896
	ds_read_b64_tr_b16 v[238:239], v131 offset:18944
	s_waitcnt lgkmcnt(6)
	v_mfma_f32_32x32x16_bf16 v[66:81], v[22:25], v[212:215], v[66:81]
	ds_read_b64_tr_b16 v[198:199], v131 offset:20992
	ds_read_b64_tr_b16 v[200:201], v131 offset:23040
	s_waitcnt lgkmcnt(6)
	v_mfma_f32_32x32x16_bf16 v[66:81], v[26:29], v[216:219], v[66:81]
	ds_read_b64_tr_b16 v[212:213], v131 offset:25088
	ds_read_b64_tr_b16 v[214:215], v131 offset:27136
	s_waitcnt lgkmcnt(6)
	v_mfma_f32_32x32x16_bf16 v[66:81], v[30:33], v[220:223], v[66:81]
	ds_read_b64_tr_b16 v[216:217], v131 offset:29184
	ds_read_b64_tr_b16 v[218:219], v131 offset:31232
	v_max3_f32 v152, v98, v99, v100
	s_waitcnt lgkmcnt(6)
	v_mfma_f32_32x32x16_bf16 v[50:65], v[18:21], v[236:239], v[50:65]
	ds_read_b64_tr_b16 v[220:221], v131 offset:17408
	ds_read_b64_tr_b16 v[222:223], v131 offset:19456
	v_max3_f32 v174, v114, v115, v116
	s_waitcnt lgkmcnt(6)
	v_mfma_f32_32x32x16_bf16 v[50:65], v[22:25], v[198:201], v[50:65]
	ds_read_b64_tr_b16 v[236:237], v131 offset:21504
	ds_read_b64_tr_b16 v[238:239], v131 offset:23552
	v_max3_f32 v152, v152, v101, v102
	s_waitcnt lgkmcnt(6)
	v_mfma_f32_32x32x16_bf16 v[50:65], v[26:29], v[212:215], v[50:65]
	ds_read_b64_tr_b16 v[198:199], v131 offset:25600
	ds_read_b64_tr_b16 v[200:201], v131 offset:27648
	v_max3_f32 v174, v174, v117, v118
	s_waitcnt lgkmcnt(6)
	v_mfma_f32_32x32x16_bf16 v[50:65], v[30:33], v[216:219], v[50:65]
	ds_read_b64_tr_b16 v[212:213], v131 offset:29696
	ds_read_b64_tr_b16 v[214:215], v131 offset:31744
	v_max3_f32 v152, v152, v103, v104
	s_waitcnt lgkmcnt(6)
	v_mfma_f32_32x32x16_bf16 v[34:49], v[18:21], v[220:223], v[34:49]
	ds_read_b64_tr_b16 v[216:217], v131 offset:17920
	ds_read_b64_tr_b16 v[218:219], v131 offset:19968
	v_max3_f32 v174, v174, v119, v120
	s_waitcnt lgkmcnt(6)
	v_mfma_f32_32x32x16_bf16 v[34:49], v[22:25], v[236:239], v[34:49]
	ds_read_b64_tr_b16 v[220:221], v131 offset:22016
	ds_read_b64_tr_b16 v[222:223], v131 offset:24064
	v_max3_f32 v152, v152, v105, v106
	s_waitcnt lgkmcnt(6)
	v_mfma_f32_32x32x16_bf16 v[34:49], v[26:29], v[198:201], v[34:49]
	ds_read_b64_tr_b16 v[236:237], v131 offset:26112
	ds_read_b64_tr_b16 v[238:239], v131 offset:28160
	v_max3_f32 v174, v174, v121, v122
	s_waitcnt lgkmcnt(6)
	v_mfma_f32_32x32x16_bf16 v[34:49], v[30:33], v[212:215], v[34:49]
	ds_read_b64_tr_b16 v[198:199], v131 offset:30208
	ds_read_b64_tr_b16 v[200:201], v131 offset:32256
	v_max3_f32 v152, v152, v107, v108
	s_waitcnt lgkmcnt(6)
	v_mfma_f32_32x32x16_bf16 v[2:17], v[18:21], v[216:219], v[2:17]
	v_max3_f32 v174, v174, v123, v124
	s_min_u32 s14, s90, 0x7c
	s_lshl_b32 s14, s14, 17
	s_add_i32 s19, s14, 0x60000
	s_add_i32 s92, s36, 0xffff0000
	s_mov_b32 s14, s10
	s_mov_b32 s15, s11
	buffer_load_dwordx4 v[224:227], v171, s[8:11], s19 offen
	s_waitcnt lgkmcnt(4)
	v_mfma_f32_32x32x16_bf16 v[2:17], v[22:25], v[220:223], v[2:17]
	v_max3_f32 v152, v152, v109, v110
	buffer_load_dwordx4 v[228:231], v172, s[12:15], s92 offen
	s_waitcnt lgkmcnt(2)
	v_mfma_f32_32x32x16_bf16 v[2:17], v[26:29], v[236:239], v[2:17]
	v_max3_f32 v174, v174, v125, v126
	buffer_load_dwordx4 v[232:235], v172, s[12:15], s36 offen
	s_waitcnt lgkmcnt(0)
	v_mfma_f32_32x32x16_bf16 v[2:17], v[30:33], v[198:201], v[2:17]
	v_max3_f32 v152, v152, v111, v112
	v_mfma_f32_4x4x4_16b_bf16 v[240:243], v[18:19], v[132:133], v[240:243]
	v_max3_f32 v174, v174, v127, v128
	v_mfma_f32_4x4x4_16b_bf16 v[244:247], v[20:21], v[132:133], v[244:247]
	v_mfma_f32_4x4x4_16b_bf16 v[240:243], v[22:23], v[132:133], v[240:243]
	v_max_f32 v152, v152, v113
	v_mfma_f32_4x4x4_16b_bf16 v[244:247], v[24:25], v[132:133], v[244:247]
	v_mfma_f32_4x4x4_16b_bf16 v[240:243], v[26:27], v[132:133], v[240:243]
	v_max_f32 v174, v174, v129
	v_mfma_f32_4x4x4_16b_bf16 v[244:247], v[28:29], v[132:133], v[244:247]
	v_mfma_f32_4x4x4_16b_bf16 v[240:243], v[30:31], v[132:133], v[240:243]
	v_max_f32 v174, v174, v152
	v_mfma_f32_4x4x4_16b_bf16 v[244:247], v[32:33], v[132:133], v[244:247]
	s_setprio 0
	s_barrier
	s_add_i32 s36, s36, 0x20000
	s_add_i32 s90, s90, 1
	s_cmpk_eq_i32 s90, 0x7e
	s_cbranch_scc1 .Lu3_exit_b2_0

; #define ATT_SBAR() __builtin_amdgcn_sched_barrier(0)
; #define ATT_PK4(P, BASE, OUT) do { u32x4 w = {cvtpk(P[BASE + 0], P[BASE + 1]), cvtpk(P[BASE + 2], P[BASE + 3]), cvtpk(P[BASE + 4], P[BASE + 5]), cvtpk(P[BASE + 6], P[BASE + 7])}; \
;     OUT = *reinterpret_cast<bf16x8*>(&w); } while (0)
; #define ATT_WRITE_K(so) do { *(bf16x8*)(K_lds + (so) + kswz<DQK>(kr, kc * 2)) = sk0; if constexpr (DQK == 128) *(bf16x8*)(K_lds + (so) + kswz<DQK>(32 + kr, kc * 2)) = sk1; } while (0)
; #define ATT_WRITE_V(so) do { *(bf16x8*)(V_lds + (so) + vst0) = sv0; *(bf16x8*)(V_lds + (so) + vst1) = sv1; } while (0)
; #define ATT_BAR() do { ATT_SBAR(); asm volatile("s_barrier" ::: "memory"); ATT_SBAR(); } while (0)
; #define ATT_VPAIR(buf, so, blk, ks) do { if constexpr (!(ABL & 8) && !(ABL & 32)) { buf[2 * (ks)] = vtr(vq0 + (so) + v_rd_off(blk, ks, 0)); buf[2 * (ks) + 1] = vtr(vq0 + (so) + v_rd_off(blk, ks, 1)); } } while (0)
; __device__ __forceinline__ void softmax_exp_pack(f32x16& p0, f32x16& p1, bf16x8& pa0, bf16x8& pa1, bf16x8& pa2, bf16x8& pa3) {
; #pragma unroll
;   for (int r = 0; r < 16; ++r) { p0[r] = __builtin_amdgcn_exp2f(p0[r]); p1[r] = __builtin_amdgcn_exp2f(p1[r]); }
;     ...
;   ATT_PK4(p0, 0, pa0); ATT_PK4(p0, 8, pa1); ATT_PK4(p1, 0, pa2); ATT_PK4(p1, 8, pa3);
;     ...
;     if constexpr (!(ABL & 4)) { ATT_WRITE_K(k2); ATT_WRITE_V(v1); }
;     ATT_SBAR();
; #pragma unroll
;     for (int ks = 0; ks < 4; ++ks) ATT_VPAIR(va, v0, 0, ks);
;     asm volatile("s_waitcnt lgkmcnt(8)" ::: "memory"); ATT_BAR();
.Lu3_join_b2_1:
	v_exp_f32_e32 v98, v98
	v_exp_f32_e32 v114, v114
	v_exp_f32_e32 v99, v99
	v_exp_f32_e32 v115, v115
	v_exp_f32_e32 v100, v100
	v_exp_f32_e32 v101, v101
	v_exp_f32_e32 v102, v102
	v_exp_f32_e32 v103, v103
	v_exp_f32_e32 v106, v106
	v_exp_f32_e32 v107, v107
	v_exp_f32_e32 v116, v116
	v_exp_f32_e32 v117, v117
	v_exp_f32_e32 v118, v118
	v_exp_f32_e32 v119, v119
	v_exp_f32_e32 v104, v104
	v_exp_f32_e32 v120, v120
	v_exp_f32_e32 v105, v105
	v_exp_f32_e32 v121, v121
	v_exp_f32_e32 v122, v122
	v_exp_f32_e32 v123, v123
	v_exp_f32_e32 v108, v108
	v_exp_f32_e32 v124, v124
	v_exp_f32_e32 v109, v109
	v_exp_f32_e32 v125, v125
	v_exp_f32_e32 v110, v110
	v_exp_f32_e32 v126, v126
	v_exp_f32_e32 v111, v111
	v_exp_f32_e32 v127, v127
	v_exp_f32_e32 v112, v112
	v_exp_f32_e32 v128, v128
	v_exp_f32_e32 v113, v113
	v_exp_f32_e32 v129, v129
	v_cvt_pk_bf16_f32 v18, v98, v99
	v_cvt_pk_bf16_f32 v19, v100, v101
	v_cvt_pk_bf16_f32 v20, v102, v103
	v_cvt_pk_bf16_f32 v22, v106, v107
	v_cvt_pk_bf16_f32 v26, v114, v115
	v_cvt_pk_bf16_f32 v21, v104, v105
	v_cvt_pk_bf16_f32 v23, v108, v109
	v_cvt_pk_bf16_f32 v24, v110, v111
	v_cvt_pk_bf16_f32 v25, v112, v113
	v_cvt_pk_bf16_f32 v27, v116, v117
	v_cvt_pk_bf16_f32 v28, v118, v119
	v_cvt_pk_bf16_f32 v29, v120, v121
	v_cvt_pk_bf16_f32 v30, v122, v123
	v_cvt_pk_bf16_f32 v31, v124, v125
	v_cvt_pk_bf16_f32 v32, v126, v127
	v_cvt_pk_bf16_f32 v33, v128, v129
	s_waitcnt vmcnt(0)
	ds_write_b128 v248, v[224:227] offset:25600
	ds_write_b128 v168, v[228:231]
	ds_write_b128 v169, v[232:235]
	ds_read_b128 v[152:155], v249 offset:16384
	ds_read_b128 v[156:159], v249 offset:20992
	ds_read_b128 v[160:163], v249 offset:16416
	ds_read_b128 v[176:179], v249 offset:21024
	s_waitcnt lgkmcnt(4)
	s_barrier
; #define ATT_SBAR() __builtin_amdgcn_sched_barrier(0)
; __device__ __forceinline__ float softmax_rowmax(const f32x16& p0, const f32x16& p1) {
;   const float m0 = p1[0] + 0.0f; float a, b;
;   asm("v_max3_f32 %0, %1, %2, %3\n\tv_max3_f32 %0, %0, %4, %5\n\tv_max3_f32 %0, %0, %6, %7\n\tv_max3_f32 %0, %0, %8, %9\n\t"
;       "v_max3_f32 %0, %0, %10, %11\n\tv_max3_f32 %0, %0, %12, %13\n\tv_max3_f32 %0, %0, %14, %15\n\tv_max3_f32 %0, %0, %16, %17"
;       : "=&v"(a) : "v"(m0), "v"(p0[0]), "v"(p0[1]), "v"(p0[2]), "v"(p0[3]), "v"(p0[4]), "v"(p0[5]), "v"(p0[6]), "v"(p0[7]), "v"(p0[8]), "v"(p0[9]), "v"(p0[10]), "v"(p0[11]), "v"(p0[12]), "v"(p0[13]), "v"(p0[14]), "v"(p0[15]));
;   asm("v_max3_f32 %0, %1, %2, %3\n\tv_max3_f32 %0, %0, %4, %5\n\tv_max3_f32 %0, %0, %6, %7\n\tv_max3_f32 %0, %0, %8, %9\n\t"
;       "v_max3_f32 %0, %0, %10, %11\n\tv_max3_f32 %0, %0, %12, %13\n\tv_max3_f32 %0, %0, %14, %15\n\tv_max_f32 %0, %0, %16"
;       : "=&v"(b) : "v"(a), "v"(p1[1]), "v"(p1[2]), "v"(p1[3]), "v"(p1[4]), "v"(p1[5]), "v"(p1[6]), "v"(p1[7]), "v"(p1[8]), "v"(p1[9]), "v"(p1[10]), "v"(p1[11]), "v"(p1[12]), "v"(p1[13]), "v"(p1[14]), "v"(p1[15]));
;   return b;
;     ...
;   for (int t = 0; t + 1 < NT; ++t) {
;     if constexpr (ABL & 1) { u32x4 w0 = {cvtpk(p0[0], p0[1]), cvtpk(p0[2], p0[3]), cvtpk(p0[4], p0[5]), cvtpk(p0[6], p0[7])}, w1 = {cvtpk(p0[8], p0[9]), cvtpk(p0[10], p0[11]), cvtpk(p0[12], p0[13]), cvtpk(p0[14], p0[15])};
;         u32x4 w2 = {cvtpk(p1[0], p1[1]), cvtpk(p1[2], p1[3]), cvtpk(p1[4], p1[5]), cvtpk(p1[6], p1[7])}, w3 = {cvtpk(p1[8], p1[9]), cvtpk(p1[10], p1[11]), cvtpk(p1[12], p1[13]), cvtpk(p1[14], p1[15])};
;         pa0 = *reinterpret_cast<bf16x8*>(&w0); pa1 = *reinterpret_cast<bf16x8*>(&w1); pa2 = *reinterpret_cast<bf16x8*>(&w2); pa3 = *reinterpret_cast<bf16x8*>(&w3); }
;     else { ATT_SOFTMAX(t == 0); }
;     if constexpr (!(ABL & 4)) { ATT_WRITE_K(k2); ATT_WRITE_V(v1); }
;     ATT_SBAR();
; #pragma unroll
;     for (int ks = 0; ks < 4; ++ks) ATT_VPAIR(va, v0, 0, ks);
;     asm volatile("s_waitcnt lgkmcnt(8)" ::: "memory"); ATT_BAR();
;     ATT_XSECTION(true);
;     if constexpr (!(ABL & 4)) { const int tk = (t + 3 < NT) ? t + 3 : NT - 1, tv = (t + 2 < NT) ? t + 2 : NT - 1; ATT_LOAD_K(tk); ATT_LOAD_V(tv); }
;     ATT_BAR();
;     { const int tk_ = k0; k0 = k1; k1 = k2; k2 = tk_; const int tv_ = v0; v0 = v1; v1 = v2; v2 = tv_; }
	s_setprio 2
	s_waitcnt lgkmcnt(3)
	v_mfma_f32_32x32x16_bf16 v[98:113], v[152:155], v[136:139], v[82:97]
	ds_read_b128 v[180:183], v249 offset:16448
	s_waitcnt lgkmcnt(3)
	v_mfma_f32_32x32x16_bf16 v[114:129], v[156:159], v[136:139], v[82:97]
	ds_read_b128 v[186:189], v249 offset:21056
	s_waitcnt lgkmcnt(3)
	v_mfma_f32_32x32x16_bf16 v[98:113], v[160:163], v[140:143], v[98:113]
	ds_read_b128 v[190:193], v249 offset:16480
	ds_read_b64_tr_b16 v[198:199], v131 offset:32768
	ds_read_b64_tr_b16 v[200:201], v131 offset:34816
	s_waitcnt lgkmcnt(5)
	v_mfma_f32_32x32x16_bf16 v[114:129], v[176:179], v[140:143], v[114:129]
	ds_read_b128 v[194:197], v249 offset:21088
	ds_read_b64_tr_b16 v[212:213], v131 offset:36864
	ds_read_b64_tr_b16 v[214:215], v131 offset:38912
	s_waitcnt lgkmcnt(7)
	v_mfma_f32_32x32x16_bf16 v[98:113], v[180:183], v[144:147], v[98:113]
	ds_read_b64_tr_b16 v[216:217], v131 offset:40960
	ds_read_b64_tr_b16 v[218:219], v131 offset:43008
	s_waitcnt lgkmcnt(8)
	v_mfma_f32_32x32x16_bf16 v[114:129], v[186:189], v[144:147], v[114:129]
	ds_read_b64_tr_b16 v[220:221], v131 offset:45056
	ds_read_b64_tr_b16 v[222:223], v131 offset:47104
	s_waitcnt lgkmcnt(9)
	v_mfma_f32_32x32x16_bf16 v[98:113], v[190:193], v[148:151], v[98:113]
	s_waitcnt lgkmcnt(6)
	v_mfma_f32_32x32x16_bf16 v[114:129], v[194:197], v[148:151], v[114:129]
	v_mfma_f32_32x32x16_bf16 v[66:81], v[18:21], v[198:201], v[66:81]
	ds_read_b64_tr_b16 v[236:237], v131 offset:33280
	ds_read_b64_tr_b16 v[238:239], v131 offset:35328
	s_waitcnt lgkmcnt(6)
	v_mfma_f32_32x32x16_bf16 v[66:81], v[22:25], v[212:215], v[66:81]
	ds_read_b64_tr_b16 v[198:199], v131 offset:37376
	ds_read_b64_tr_b16 v[200:201], v131 offset:39424
	s_waitcnt lgkmcnt(6)
	v_mfma_f32_32x32x16_bf16 v[66:81], v[26:29], v[216:219], v[66:81]
	ds_read_b64_tr_b16 v[212:213], v131 offset:41472
	ds_read_b64_tr_b16 v[214:215], v131 offset:43520
	s_waitcnt lgkmcnt(6)
	v_mfma_f32_32x32x16_bf16 v[66:81], v[30:33], v[220:223], v[66:81]
	ds_read_b64_tr_b16 v[216:217], v131 offset:45568
	ds_read_b64_tr_b16 v[218:219], v131 offset:47616
	v_max3_f32 v152, v98, v99, v100
	s_waitcnt lgkmcnt(6)
	v_mfma_f32_32x32x16_bf16 v[50:65], v[18:21], v[236:239], v[50:65]
	ds_read_b64_tr_b16 v[220:221], v131 offset:33792
	ds_read_b64_tr_b16 v[222:223], v131 offset:35840
	v_max3_f32 v174, v114, v115, v116
	s_waitcnt lgkmcnt(6)
	v_mfma_f32_32x32x16_bf16 v[50:65], v[22:25], v[198:201], v[50:65]
	ds_read_b64_tr_b16 v[236:237], v131 offset:37888
	ds_read_b64_tr_b16 v[238:239], v131 offset:39936
	v_max3_f32 v152, v152, v101, v102
	s_waitcnt lgkmcnt(6)
	v_mfma_f32_32x32x16_bf16 v[50:65], v[26:29], v[212:215], v[50:65]
	ds_read_b64_tr_b16 v[198:199], v131 offset:41984
	ds_read_b64_tr_b16 v[200:201], v131 offset:44032
	v_max3_f32 v174, v174, v117, v118
	s_waitcnt lgkmcnt(6)
	v_mfma_f32_32x32x16_bf16 v[50:65], v[30:33], v[216:219], v[50:65]
	ds_read_b64_tr_b16 v[212:213], v131 offset:46080
	ds_read_b64_tr_b16 v[214:215], v131 offset:48128
	v_max3_f32 v152, v152, v103, v104
	s_waitcnt lgkmcnt(6)
	v_mfma_f32_32x32x16_bf16 v[34:49], v[18:21], v[220:223], v[34:49]
	ds_read_b64_tr_b16 v[216:217], v131 offset:34304
	ds_read_b64_tr_b16 v[218:219], v131 offset:36352
	v_max3_f32 v174, v174, v119, v120
	s_waitcnt lgkmcnt(6)
	v_mfma_f32_32x32x16_bf16 v[34:49], v[22:25], v[236:239], v[34:49]
	ds_read_b64_tr_b16 v[220:221], v131 offset:38400
	ds_read_b64_tr_b16 v[222:223], v131 offset:40448
	v_max3_f32 v152, v152, v105, v106
	s_waitcnt lgkmcnt(6)
	v_mfma_f32_32x32x16_bf16 v[34:49], v[26:29], v[198:201], v[34:49]
	ds_read_b64_tr_b16 v[236:237], v131 offset:42496
	ds_read_b64_tr_b16 v[238:239], v131 offset:44544
	v_max3_f32 v174, v174, v121, v122
	s_waitcnt lgkmcnt(6)
	v_mfma_f32_32x32x16_bf16 v[34:49], v[30:33], v[212:215], v[34:49]
	ds_read_b64_tr_b16 v[198:199], v131 offset:46592
	ds_read_b64_tr_b16 v[200:201], v131 offset:48640
	v_max3_f32 v152, v152, v107, v108
	s_waitcnt lgkmcnt(6)
	v_mfma_f32_32x32x16_bf16 v[2:17], v[18:21], v[216:219], v[2:17]
	v_max3_f32 v174, v174, v123, v124
	s_min_u32 s14, s90, 0x7c
	s_lshl_b32 s14, s14, 17
	s_add_i32 s19, s14, 0x60000
	s_add_i32 s92, s36, 0xffff0000
	s_mov_b32 s14, s10
	s_mov_b32 s15, s11
	buffer_load_dwordx4 v[224:227], v171, s[8:11], s19 offen
	s_waitcnt lgkmcnt(4)
	v_mfma_f32_32x32x16_bf16 v[2:17], v[22:25], v[220:223], v[2:17]
	v_max3_f32 v152, v152, v109, v110
	buffer_load_dwordx4 v[228:231], v172, s[12:15], s92 offen
	s_waitcnt lgkmcnt(2)
	v_mfma_f32_32x32x16_bf16 v[2:17], v[26:29], v[236:239], v[2:17]
	v_max3_f32 v174, v174, v125, v126
	buffer_load_dwordx4 v[232:235], v172, s[12:15], s36 offen
	s_waitcnt lgkmcnt(0)
	v_mfma_f32_32x32x16_bf16 v[2:17], v[30:33], v[198:201], v[2:17]
	v_max3_f32 v152, v152, v111, v112
	v_mfma_f32_4x4x4_16b_bf16 v[240:243], v[18:19], v[132:133], v[240:243]
	v_max3_f32 v174, v174, v127, v128
	v_mfma_f32_4x4x4_16b_bf16 v[244:247], v[20:21], v[132:133], v[244:247]
	v_mfma_f32_4x4x4_16b_bf16 v[240:243], v[22:23], v[132:133], v[240:243]
	v_max_f32 v152, v152, v113
	v_mfma_f32_4x4x4_16b_bf16 v[244:247], v[24:25], v[132:133], v[244:247]
	v_mfma_f32_4x4x4_16b_bf16 v[240:243], v[26:27], v[132:133], v[240:243]
	v_max_f32 v174, v174, v129
	v_mfma_f32_4x4x4_16b_bf16 v[244:247], v[28:29], v[132:133], v[244:247]
	v_mfma_f32_4x4x4_16b_bf16 v[240:243], v[30:31], v[132:133], v[240:243]
	v_max_f32 v174, v174, v152
	v_mfma_f32_4x4x4_16b_bf16 v[244:247], v[32:33], v[132:133], v[244:247]
	s_setprio 0
	s_barrier
	s_add_i32 s36, s36, 0x20000
	s_add_i32 s90, s90, 1
	s_cmpk_eq_i32 s90, 0x7e
	s_cbranch_scc1 .Lu3_exit_b2_1

; #define ATT_SBAR() __builtin_amdgcn_sched_barrier(0)
; #define ATT_PK4(P, BASE, OUT) do { u32x4 w = {cvtpk(P[BASE + 0], P[BASE + 1]), cvtpk(P[BASE + 2], P[BASE + 3]), cvtpk(P[BASE + 4], P[BASE + 5]), cvtpk(P[BASE + 6], P[BASE + 7])}; \
;     OUT = *reinterpret_cast<bf16x8*>(&w); } while (0)
; #define ATT_WRITE_K(so) do { *(bf16x8*)(K_lds + (so) + kswz<DQK>(kr, kc * 2)) = sk0; if constexpr (DQK == 128) *(bf16x8*)(K_lds + (so) + kswz<DQK>(32 + kr, kc * 2)) = sk1; } while (0)
; #define ATT_WRITE_V(so) do { *(bf16x8*)(V_lds + (so) + vst0) = sv0; *(bf16x8*)(V_lds + (so) + vst1) = sv1; } while (0)
; #define ATT_BAR() do { ATT_SBAR(); asm volatile("s_barrier" ::: "memory"); ATT_SBAR(); } while (0)
; #define ATT_VPAIR(buf, so, blk, ks) do { if constexpr (!(ABL & 8) && !(ABL & 32)) { buf[2 * (ks)] = vtr(vq0 + (so) + v_rd_off(blk, ks, 0)); buf[2 * (ks) + 1] = vtr(vq0 + (so) + v_rd_off(blk, ks, 1)); } } while (0)
; __device__ __forceinline__ void softmax_exp_pack(f32x16& p0, f32x16& p1, bf16x8& pa0, bf16x8& pa1, bf16x8& pa2, bf16x8& pa3) {
; #pragma unroll
;   for (int r = 0; r < 16; ++r) { p0[r] = __builtin_amdgcn_exp2f(p0[r]); p1[r] = __builtin_amdgcn_exp2f(p1[r]); }
;     ...
;   ATT_PK4(p0, 0, pa0); ATT_PK4(p0, 8, pa1); ATT_PK4(p1, 0, pa2); ATT_PK4(p1, 8, pa3);
;     ...
;     if constexpr (!(ABL & 4)) { ATT_WRITE_K(k2); ATT_WRITE_V(v1); }
;     ATT_SBAR();
; #pragma unroll
;     for (int ks = 0; ks < 4; ++ks) ATT_VPAIR(va, v0, 0, ks);
;     asm volatile("s_waitcnt lgkmcnt(8)" ::: "memory"); ATT_BAR();
.Lu3_join_b2_2:
	v_exp_f32_e32 v98, v98
	v_exp_f32_e32 v114, v114
	v_exp_f32_e32 v99, v99
	v_exp_f32_e32 v115, v115
	v_exp_f32_e32 v100, v100
	v_exp_f32_e32 v101, v101
	v_exp_f32_e32 v102, v102
	v_exp_f32_e32 v103, v103
	v_exp_f32_e32 v106, v106
	v_exp_f32_e32 v107, v107
	v_exp_f32_e32 v116, v116
	v_exp_f32_e32 v117, v117
	v_exp_f32_e32 v118, v118
	v_exp_f32_e32 v119, v119
	v_exp_f32_e32 v104, v104
	v_exp_f32_e32 v120, v120
	v_exp_f32_e32 v105, v105
	v_exp_f32_e32 v121, v121
	v_exp_f32_e32 v122, v122
	v_exp_f32_e32 v123, v123
	v_exp_f32_e32 v108, v108
	v_exp_f32_e32 v124, v124
	v_exp_f32_e32 v109, v109
	v_exp_f32_e32 v125, v125
	v_exp_f32_e32 v110, v110
	v_exp_f32_e32 v126, v126
	v_exp_f32_e32 v111, v111
	v_exp_f32_e32 v127, v127
	v_exp_f32_e32 v112, v112
	v_exp_f32_e32 v128, v128
	v_exp_f32_e32 v113, v113
	v_exp_f32_e32 v129, v129
	v_cvt_pk_bf16_f32 v18, v98, v99
	v_cvt_pk_bf16_f32 v19, v100, v101
	v_cvt_pk_bf16_f32 v20, v102, v103
	v_cvt_pk_bf16_f32 v22, v106, v107
	v_cvt_pk_bf16_f32 v26, v114, v115
	v_cvt_pk_bf16_f32 v21, v104, v105
	v_cvt_pk_bf16_f32 v23, v108, v109
	v_cvt_pk_bf16_f32 v24, v110, v111
	v_cvt_pk_bf16_f32 v25, v112, v113
	v_cvt_pk_bf16_f32 v27, v116, v117
	v_cvt_pk_bf16_f32 v28, v118, v119
	v_cvt_pk_bf16_f32 v29, v120, v121
	v_cvt_pk_bf16_f32 v30, v122, v123
	v_cvt_pk_bf16_f32 v31, v124, v125
	v_cvt_pk_bf16_f32 v32, v126, v127
	v_cvt_pk_bf16_f32 v33, v128, v129
	s_waitcnt vmcnt(0)
	ds_write_b128 v248, v[224:227] offset:34816
	ds_write_b128 v168, v[228:231] offset:16384
	ds_write_b128 v169, v[232:235] offset:16384
	ds_read_b128 v[152:155], v249 offset:25600
	ds_read_b128 v[156:159], v249 offset:30208
	ds_read_b128 v[160:163], v249 offset:25632
	ds_read_b128 v[176:179], v249 offset:30240
	s_waitcnt lgkmcnt(4)
	s_barrier
; #define ATT_SBAR() __builtin_amdgcn_sched_barrier(0)
; __device__ __forceinline__ float softmax_rowmax(const f32x16& p0, const f32x16& p1) {
;   const float m0 = p1[0] + 0.0f; float a, b;
;   asm("v_max3_f32 %0, %1, %2, %3\n\tv_max3_f32 %0, %0, %4, %5\n\tv_max3_f32 %0, %0, %6, %7\n\tv_max3_f32 %0, %0, %8, %9\n\t"
;       "v_max3_f32 %0, %0, %10, %11\n\tv_max3_f32 %0, %0, %12, %13\n\tv_max3_f32 %0, %0, %14, %15\n\tv_max3_f32 %0, %0, %16, %17"
;       : "=&v"(a) : "v"(m0), "v"(p0[0]), "v"(p0[1]), "v"(p0[2]), "v"(p0[3]), "v"(p0[4]), "v"(p0[5]), "v"(p0[6]), "v"(p0[7]), "v"(p0[8]), "v"(p0[9]), "v"(p0[10]), "v"(p0[11]), "v"(p0[12]), "v"(p0[13]), "v"(p0[14]), "v"(p0[15]));
;   asm("v_max3_f32 %0, %1, %2, %3\n\tv_max3_f32 %0, %0, %4, %5\n\tv_max3_f32 %0, %0, %6, %7\n\tv_max3_f32 %0, %0, %8, %9\n\t"
;       "v_max3_f32 %0, %0, %10, %11\n\tv_max3_f32 %0, %0, %12, %13\n\tv_max3_f32 %0, %0, %14, %15\n\tv_max_f32 %0, %0, %16"
;       : "=&v"(b) : "v"(a), "v"(p1[1]), "v"(p1[2]), "v"(p1[3]), "v"(p1[4]), "v"(p1[5]), "v"(p1[6]), "v"(p1[7]), "v"(p1[8]), "v"(p1[9]), "v"(p1[10]), "v"(p1[11]), "v"(p1[12]), "v"(p1[13]), "v"(p1[14]), "v"(p1[15]));
;   return b;
;     ...
;   for (int t = 0; t + 1 < NT; ++t) {
;     if constexpr (ABL & 1) { u32x4 w0 = {cvtpk(p0[0], p0[1]), cvtpk(p0[2], p0[3]), cvtpk(p0[4], p0[5]), cvtpk(p0[6], p0[7])}, w1 = {cvtpk(p0[8], p0[9]), cvtpk(p0[10], p0[11]), cvtpk(p0[12], p0[13]), cvtpk(p0[14], p0[15])};
;         u32x4 w2 = {cvtpk(p1[0], p1[1]), cvtpk(p1[2], p1[3]), cvtpk(p1[4], p1[5]), cvtpk(p1[6], p1[7])}, w3 = {cvtpk(p1[8], p1[9]), cvtpk(p1[10], p1[11]), cvtpk(p1[12], p1[13]), cvtpk(p1[14], p1[15])};
;         pa0 = *reinterpret_cast<bf16x8*>(&w0); pa1 = *reinterpret_cast<bf16x8*>(&w1); pa2 = *reinterpret_cast<bf16x8*>(&w2); pa3 = *reinterpret_cast<bf16x8*>(&w3); }
;     else { ATT_SOFTMAX(t == 0); }
;     if constexpr (!(ABL & 4)) { ATT_WRITE_K(k2); ATT_WRITE_V(v1); }
;     ATT_SBAR();
; #pragma unroll
;     for (int ks = 0; ks < 4; ++ks) ATT_VPAIR(va, v0, 0, ks);
;     asm volatile("s_waitcnt lgkmcnt(8)" ::: "memory"); ATT_BAR();
;     ATT_XSECTION(true);
;     if constexpr (!(ABL & 4)) { const int tk = (t + 3 < NT) ? t + 3 : NT - 1, tv = (t + 2 < NT) ? t + 2 : NT - 1; ATT_LOAD_K(tk); ATT_LOAD_V(tv); }
;     ATT_BAR();
;     { const int tk_ = k0; k0 = k1; k1 = k2; k2 = tk_; const int tv_ = v0; v0 = v1; v1 = v2; v2 = tv_; }
;   }
	s_setprio 2
	s_waitcnt lgkmcnt(3)
	v_mfma_f32_32x32x16_bf16 v[98:113], v[152:155], v[136:139], v[82:97]
	ds_read_b128 v[180:183], v249 offset:25664
	s_waitcnt lgkmcnt(3)
	v_mfma_f32_32x32x16_bf16 v[114:129], v[156:159], v[136:139], v[82:97]
	ds_read_b128 v[186:189], v249 offset:30272
	s_waitcnt lgkmcnt(3)
	v_mfma_f32_32x32x16_bf16 v[98:113], v[160:163], v[140:143], v[98:113]
	ds_read_b128 v[190:193], v249 offset:25696
	ds_read_b64_tr_b16 v[198:199], v131
	ds_read_b64_tr_b16 v[200:201], v131 offset:2048
	s_waitcnt lgkmcnt(5)
	v_mfma_f32_32x32x16_bf16 v[114:129], v[176:179], v[140:143], v[114:129]
	ds_read_b128 v[194:197], v249 offset:30304
	ds_read_b64_tr_b16 v[212:213], v131 offset:4096
	ds_read_b64_tr_b16 v[214:215], v131 offset:6144
	s_waitcnt lgkmcnt(7)
	v_mfma_f32_32x32x16_bf16 v[98:113], v[180:183], v[144:147], v[98:113]
	ds_read_b64_tr_b16 v[216:217], v131 offset:8192
	ds_read_b64_tr_b16 v[218:219], v131 offset:10240
	s_waitcnt lgkmcnt(8)
	v_mfma_f32_32x32x16_bf16 v[114:129], v[186:189], v[144:147], v[114:129]
	ds_read_b64_tr_b16 v[220:221], v131 offset:12288
	ds_read_b64_tr_b16 v[222:223], v131 offset:14336
	s_waitcnt lgkmcnt(9)
	v_mfma_f32_32x32x16_bf16 v[98:113], v[190:193], v[148:151], v[98:113]
	s_waitcnt lgkmcnt(6)
	v_mfma_f32_32x32x16_bf16 v[114:129], v[194:197], v[148:151], v[114:129]
	v_mfma_f32_32x32x16_bf16 v[66:81], v[18:21], v[198:201], v[66:81]
	ds_read_b64_tr_b16 v[236:237], v131 offset:512
	ds_read_b64_tr_b16 v[238:239], v131 offset:2560
	s_waitcnt lgkmcnt(6)
	v_mfma_f32_32x32x16_bf16 v[66:81], v[22:25], v[212:215], v[66:81]
	ds_read_b64_tr_b16 v[198:199], v131 offset:4608
	ds_read_b64_tr_b16 v[200:201], v131 offset:6656
	s_waitcnt lgkmcnt(6)
	v_mfma_f32_32x32x16_bf16 v[66:81], v[26:29], v[216:219], v[66:81]
	ds_read_b64_tr_b16 v[212:213], v131 offset:8704
	ds_read_b64_tr_b16 v[214:215], v131 offset:10752
	s_waitcnt lgkmcnt(6)
	v_mfma_f32_32x32x16_bf16 v[66:81], v[30:33], v[220:223], v[66:81]
	ds_read_b64_tr_b16 v[216:217], v131 offset:12800
	ds_read_b64_tr_b16 v[218:219], v131 offset:14848
	v_max3_f32 v152, v98, v99, v100
	s_waitcnt lgkmcnt(6)
	v_mfma_f32_32x32x16_bf16 v[50:65], v[18:21], v[236:239], v[50:65]
	ds_read_b64_tr_b16 v[220:221], v131 offset:1024
	ds_read_b64_tr_b16 v[222:223], v131 offset:3072
	v_max3_f32 v174, v114, v115, v116
	s_waitcnt lgkmcnt(6)
	v_mfma_f32_32x32x16_bf16 v[50:65], v[22:25], v[198:201], v[50:65]
	ds_read_b64_tr_b16 v[236:237], v131 offset:5120
	ds_read_b64_tr_b16 v[238:239], v131 offset:7168
	v_max3_f32 v152, v152, v101, v102
	s_waitcnt lgkmcnt(6)
	v_mfma_f32_32x32x16_bf16 v[50:65], v[26:29], v[212:215], v[50:65]
	ds_read_b64_tr_b16 v[198:199], v131 offset:9216
	ds_read_b64_tr_b16 v[200:201], v131 offset:11264
	v_max3_f32 v174, v174, v117, v118
	s_waitcnt lgkmcnt(6)
	v_mfma_f32_32x32x16_bf16 v[50:65], v[30:33], v[216:219], v[50:65]
	ds_read_b64_tr_b16 v[212:213], v131 offset:13312
	ds_read_b64_tr_b16 v[214:215], v131 offset:15360
	v_max3_f32 v152, v152, v103, v104
	s_waitcnt lgkmcnt(6)
	v_mfma_f32_32x32x16_bf16 v[34:49], v[18:21], v[220:223], v[34:49]
	ds_read_b64_tr_b16 v[216:217], v131 offset:1536
	ds_read_b64_tr_b16 v[218:219], v131 offset:3584
	v_max3_f32 v174, v174, v119, v120
	s_waitcnt lgkmcnt(6)
	v_mfma_f32_32x32x16_bf16 v[34:49], v[22:25], v[236:239], v[34:49]
	ds_read_b64_tr_b16 v[220:221], v131 offset:5632
	ds_read_b64_tr_b16 v[222:223], v131 offset:7680
	v_max3_f32 v152, v152, v105, v106
	s_waitcnt lgkmcnt(6)
	v_mfma_f32_32x32x16_bf16 v[34:49], v[26:29], v[198:201], v[34:49]
	ds_read_b64_tr_b16 v[236:237], v131 offset:9728
	ds_read_b64_tr_b16 v[238:239], v131 offset:11776
	v_max3_f32 v174, v174, v121, v122
	s_waitcnt lgkmcnt(6)
	v_mfma_f32_32x32x16_bf16 v[34:49], v[30:33], v[212:215], v[34:49]
	ds_read_b64_tr_b16 v[198:199], v131 offset:13824
	ds_read_b64_tr_b16 v[200:201], v131 offset:15872
	v_max3_f32 v152, v152, v107, v108
	s_waitcnt lgkmcnt(6)
	v_mfma_f32_32x32x16_bf16 v[2:17], v[18:21], v[216:219], v[2:17]
	v_max3_f32 v174, v174, v123, v124
	s_min_u32 s14, s90, 0x7c
	s_lshl_b32 s14, s14, 17
	s_add_i32 s19, s14, 0x60000
	s_add_i32 s92, s36, 0xffff0000
	s_mov_b32 s14, s10
	s_mov_b32 s15, s11
	buffer_load_dwordx4 v[224:227], v171, s[8:11], s19 offen
	s_waitcnt lgkmcnt(4)
	v_mfma_f32_32x32x16_bf16 v[2:17], v[22:25], v[220:223], v[2:17]
	v_max3_f32 v152, v152, v109, v110
	buffer_load_dwordx4 v[228:231], v172, s[12:15], s92 offen
	s_waitcnt lgkmcnt(2)
	v_mfma_f32_32x32x16_bf16 v[2:17], v[26:29], v[236:239], v[2:17]
	v_max3_f32 v174, v174, v125, v126
	buffer_load_dwordx4 v[232:235], v172, s[12:15], s36 offen
	s_waitcnt lgkmcnt(0)
	v_mfma_f32_32x32x16_bf16 v[2:17], v[30:33], v[198:201], v[2:17]
	v_max3_f32 v152, v152, v111, v112
	v_mfma_f32_4x4x4_16b_bf16 v[240:243], v[18:19], v[132:133], v[240:243]
	v_max3_f32 v174, v174, v127, v128
	v_mfma_f32_4x4x4_16b_bf16 v[244:247], v[20:21], v[132:133], v[244:247]
	v_mfma_f32_4x4x4_16b_bf16 v[240:243], v[22:23], v[132:133], v[240:243]
	v_max_f32 v152, v152, v113
	v_mfma_f32_4x4x4_16b_bf16 v[244:247], v[24:25], v[132:133], v[244:247]
	v_mfma_f32_4x4x4_16b_bf16 v[240:243], v[26:27], v[132:133], v[240:243]
	v_max_f32 v174, v174, v129
	v_mfma_f32_4x4x4_16b_bf16 v[244:247], v[28:29], v[132:133], v[244:247]
	v_mfma_f32_4x4x4_16b_bf16 v[240:243], v[30:31], v[132:133], v[240:243]
	v_max_f32 v174, v174, v152
	v_mfma_f32_4x4x4_16b_bf16 v[244:247], v[32:33], v[132:133], v[244:247]
	s_setprio 0
	s_barrier
	s_add_i32 s36, s36, 0x20000
	s_add_i32 s90, s90, 1
	s_cmpk_eq_i32 s90, 0x7e
	s_cbranch_scc1 .Lu3_exit_b2_2
	s_branch .Lu3_b2_0
.Lu3_exit_b2_0:
	s_mov_b32 s18, 0x4800
	s_mov_b32 s37, 0x4000
	s_mov_b32 s48, 0x0
	s_mov_b32 s49, 0x0
	s_mov_b32 s50, 0x8000
	s_mov_b32 s51, 0x2400
	s_branch .LBB0_305

; #define ATT_SBAR() __builtin_amdgcn_sched_barrier(0)
; __device__ __forceinline__ unsigned cvtpk(float lo, float hi) { f32x2_t v = {lo, hi}; bf16x2_t b = __builtin_convertvector(v, bf16x2_t); return __builtin_bit_cast(unsigned, b); }
; #define ATT_LOAD_K(t) do { const unsigned so_ = (unsigned)(t) * (unsigned)(KVBLK * LDK * 2); sk0 = __builtin_bit_cast(bf16x8, __builtin_amdgcn_raw_buffer_load_b128(krs, koff, so_, 0)); \
;     if constexpr (DQK == 128) sk1 = __builtin_bit_cast(bf16x8, __builtin_amdgcn_raw_buffer_load_b128(krs, koff, so_ + (unsigned)(32 * LDK * 2), 0)); } while (0)
; #define ATT_LOAD_V(t) do { const unsigned so_ = (unsigned)(t) * (unsigned)(KVBLK * LDV * 2); sv0 = __builtin_bit_cast(bf16x8, __builtin_amdgcn_raw_buffer_load_b128(vrs, voff, so_, 0)); \
;     sv1 = __builtin_bit_cast(bf16x8, __builtin_amdgcn_raw_buffer_load_b128(vrs, voff, so_ + (unsigned)(32 * LDV * 2), 0)); } while (0)
; #define ATT_WRITE_K(so) do { *(bf16x8*)(K_lds + (so) + kswz<DQK>(kr, kc * 2)) = sk0; if constexpr (DQK == 128) *(bf16x8*)(K_lds + (so) + kswz<DQK>(32 + kr, kc * 2)) = sk1; } while (0)
;     ...
;   for (int t = 0; t + 1 < NT; ++t) {
;     if constexpr (ABL & 1) { u32x4 w0 = {cvtpk(p0[0], p0[1]), cvtpk(p0[2], p0[3]), cvtpk(p0[4], p0[5]), cvtpk(p0[6], p0[7])}, w1 = {cvtpk(p0[8], p0[9]), cvtpk(p0[10], p0[11]), cvtpk(p0[12], p0[13]), cvtpk(p0[14], p0[15])};
;         u32x4 w2 = {cvtpk(p1[0], p1[1]), cvtpk(p1[2], p1[3]), cvtpk(p1[4], p1[5]), cvtpk(p1[6], p1[7])}, w3 = {cvtpk(p1[8], p1[9]), cvtpk(p1[10], p1[11]), cvtpk(p1[12], p1[13]), cvtpk(p1[14], p1[15])};
;         pa0 = *reinterpret_cast<bf16x8*>(&w0); pa1 = *reinterpret_cast<bf16x8*>(&w1); pa2 = *reinterpret_cast<bf16x8*>(&w2); pa3 = *reinterpret_cast<bf16x8*>(&w3); }
;     else { ATT_SOFTMAX(t == 0); }
;     if constexpr (!(ABL & 4)) { ATT_WRITE_K(k2); ATT_WRITE_V(v1); }
;     ATT_SBAR();
; #pragma unroll
;     for (int ks = 0; ks < 4; ++ks) ATT_VPAIR(va, v0, 0, ks);
;     asm volatile("s_waitcnt lgkmcnt(8)" ::: "memory"); ATT_BAR();
;     ATT_XSECTION(true);
;     if constexpr (!(ABL & 4)) { const int tk = (t + 3 < NT) ? t + 3 : NT - 1, tv = (t + 2 < NT) ? t + 2 : NT - 1; ATT_LOAD_K(tk); ATT_LOAD_V(tv); }
;     ATT_BAR();
;     { const int tk_ = k0; k0 = k1; k1 = k2; k2 = tk_; const int tv_ = v0; v0 = v1; v1 = v2; v2 = tv_; }
;   }
.Lu3_exit_b2_1:
	s_mov_b32 s18, 0x0
	s_mov_b32 s37, 0x8000
	s_mov_b32 s48, 0x4000
	s_mov_b32 s49, 0x2400
	s_mov_b32 s50, 0x0
	s_mov_b32 s51, 0x4800
	s_branch .LBB0_305

; #define ATT_SBAR() __builtin_amdgcn_sched_barrier(0)
; __device__ __forceinline__ unsigned cvtpk(float lo, float hi) { f32x2_t v = {lo, hi}; bf16x2_t b = __builtin_convertvector(v, bf16x2_t); return __builtin_bit_cast(unsigned, b); }
; #define ATT_LOAD_K(t) do { const unsigned so_ = (unsigned)(t) * (unsigned)(KVBLK * LDK * 2); sk0 = __builtin_bit_cast(bf16x8, __builtin_amdgcn_raw_buffer_load_b128(krs, koff, so_, 0)); \
;     if constexpr (DQK == 128) sk1 = __builtin_bit_cast(bf16x8, __builtin_amdgcn_raw_buffer_load_b128(krs, koff, so_ + (unsigned)(32 * LDK * 2), 0)); } while (0)
; #define ATT_LOAD_V(t) do { const unsigned so_ = (unsigned)(t) * (unsigned)(KVBLK * LDV * 2); sv0 = __builtin_bit_cast(bf16x8, __builtin_amdgcn_raw_buffer_load_b128(vrs, voff, so_, 0)); \
;     sv1 = __builtin_bit_cast(bf16x8, __builtin_amdgcn_raw_buffer_load_b128(vrs, voff, so_ + (unsigned)(32 * LDV * 2), 0)); } while (0)
; #define ATT_WRITE_K(so) do { *(bf16x8*)(K_lds + (so) + kswz<DQK>(kr, kc * 2)) = sk0; if constexpr (DQK == 128) *(bf16x8*)(K_lds + (so) + kswz<DQK>(32 + kr, kc * 2)) = sk1; } while (0)
;     ...
;   for (int t = 0; t + 1 < NT; ++t) {
;     if constexpr (ABL & 1) { u32x4 w0 = {cvtpk(p0[0], p0[1]), cvtpk(p0[2], p0[3]), cvtpk(p0[4], p0[5]), cvtpk(p0[6], p0[7])}, w1 = {cvtpk(p0[8], p0[9]), cvtpk(p0[10], p0[11]), cvtpk(p0[12], p0[13]), cvtpk(p0[14], p0[15])};
;         u32x4 w2 = {cvtpk(p1[0], p1[1]), cvtpk(p1[2], p1[3]), cvtpk(p1[4], p1[5]), cvtpk(p1[6], p1[7])}, w3 = {cvtpk(p1[8], p1[9]), cvtpk(p1[10], p1[11]), cvtpk(p1[12], p1[13]), cvtpk(p1[14], p1[15])};
;         pa0 = *reinterpret_cast<bf16x8*>(&w0); pa1 = *reinterpret_cast<bf16x8*>(&w1); pa2 = *reinterpret_cast<bf16x8*>(&w2); pa3 = *reinterpret_cast<bf16x8*>(&w3); }
;     else { ATT_SOFTMAX(t == 0); }
;     if constexpr (!(ABL & 4)) { ATT_WRITE_K(k2); ATT_WRITE_V(v1); }
;     ATT_SBAR();
; #pragma unroll
;     for (int ks = 0; ks < 4; ++ks) ATT_VPAIR(va, v0, 0, ks);
;     asm volatile("s_waitcnt lgkmcnt(8)" ::: "memory"); ATT_BAR();
;     ATT_XSECTION(true);
;     if constexpr (!(ABL & 4)) { const int tk = (t + 3 < NT) ? t + 3 : NT - 1, tv = (t + 2 < NT) ? t + 2 : NT - 1; ATT_LOAD_K(tk); ATT_LOAD_V(tv); }
;     ATT_BAR();
;     { const int tk_ = k0; k0 = k1; k1 = k2; k2 = tk_; const int tv_ = v0; v0 = v1; v1 = v2; v2 = tv_; }
;   }
.Lu3_exit_b2_2:
	s_mov_b32 s18, 0x2400
	s_mov_b32 s37, 0x0
	s_mov_b32 s48, 0x8000
	s_mov_b32 s49, 0x4800
	s_mov_b32 s50, 0x4000
	s_mov_b32 s51, 0x0
	s_branch .LBB0_305

; __device__ __forceinline__ float softmax_shift(f32x16& p0, f32x16& p1, f32x16& negm, float pmax, bool first) {
;   asm volatile("s_nop 4" ::: "memory");
;   { auto rr = __builtin_amdgcn_permlane32_swap(__float_as_uint(pmax), __float_as_uint(pmax), false, false);
;     pmax = fmaxf(__uint_as_float(rr[0]), __uint_as_float(rr[1])); }
;   const float delta = first ? pmax : fmaxf(pmax, 0.f);
; #pragma unroll
;   for (int r = 0; r < 16; ++r) { p0[r] -= delta; p1[r] -= delta; negm[r] -= delta; }
;   return first ? 1.f : __builtin_amdgcn_exp2f(-delta);
; }
.LBB0_304:
	v_sub_f32_e32 v113, v113, v174
	v_sub_f32_e32 v112, v112, v174
	v_sub_f32_e32 v111, v111, v174
	v_sub_f32_e32 v110, v110, v174
	v_sub_f32_e32 v109, v109, v174
	v_sub_f32_e32 v108, v108, v174
	v_sub_f32_e32 v107, v107, v174
	v_sub_f32_e32 v106, v106, v174
	v_sub_f32_e32 v105, v105, v174
	v_sub_f32_e32 v104, v104, v174
	v_sub_f32_e32 v103, v103, v174
	v_sub_f32_e32 v102, v102, v174
	v_sub_f32_e32 v101, v101, v174
	v_sub_f32_e32 v100, v100, v174
	v_sub_f32_e32 v99, v99, v174
	v_sub_f32_e32 v98, v98, v174
	v_sub_f32_e32 v129, v129, v174
	v_sub_f32_e32 v128, v128, v174
	v_sub_f32_e32 v127, v127, v174
	v_sub_f32_e32 v126, v126, v174
	v_sub_f32_e32 v125, v125, v174
	v_sub_f32_e32 v124, v124, v174
	v_sub_f32_e32 v123, v123, v174
	v_sub_f32_e32 v122, v122, v174
	v_sub_f32_e32 v121, v121, v174
	v_sub_f32_e32 v120, v120, v174
	v_sub_f32_e32 v119, v119, v174
	v_sub_f32_e32 v118, v118, v174
	v_sub_f32_e32 v117, v117, v174
	v_sub_f32_e32 v116, v116, v174
	v_sub_f32_e32 v115, v115, v174
	v_sub_f32_e32 v114, v114, v174
	v_sub_f32_e32 v97, v97, v174
	v_sub_f32_e32 v96, v96, v174
	v_sub_f32_e32 v95, v95, v174
	v_sub_f32_e32 v94, v94, v174
	v_sub_f32_e32 v93, v93, v174
	v_sub_f32_e32 v92, v92, v174
	v_sub_f32_e32 v91, v91, v174
	v_sub_f32_e32 v90, v90, v174
	v_sub_f32_e32 v89, v89, v174
	v_sub_f32_e32 v88, v88, v174
	v_sub_f32_e32 v87, v87, v174
	v_sub_f32_e32 v86, v86, v174
	v_sub_f32_e32 v85, v85, v174
	v_sub_f32_e32 v84, v84, v174
	v_sub_f32_e32 v83, v83, v174
	v_sub_f32_e32 v82, v82, v174
	s_cmp_eq_u32 s101, 0
	s_cbranch_scc1 .LBB0_298
	s_cmp_eq_u32 s101, 1
	s_cbranch_scc1 .Lu3_join_b2_1
	s_branch .Lu3_join_b2_2

; __global__ void __launch_bounds__(NWAVES * 64, 2) fwd_kernel(Args args) {
;     extern __shared__ __attribute__((aligned(16))) unsigned char lds[];
;     Frame F;
;     F.lds = lds; F.tid = threadIdx.x; F.lane = F.tid & 63; F.wave = __builtin_amdgcn_readfirstlane(F.tid >> 6);
	.amdhsa_kernel _Z10fwd_kernel4Args
		.amdhsa_group_segment_fixed_size 0
		.amdhsa_private_segment_fixed_size 0
		.amdhsa_kernarg_size 464
		.amdhsa_user_sgpr_count 2
		.amdhsa_user_sgpr_dispatch_ptr 0
		.amdhsa_user_sgpr_queue_ptr 0
		.amdhsa_user_sgpr_kernarg_segment_ptr 1
		.amdhsa_user_sgpr_dispatch_id 0
		.amdhsa_user_sgpr_kernarg_preload_length 0
		.amdhsa_user_sgpr_kernarg_preload_offset 0
		.amdhsa_user_sgpr_private_segment_size 0
		.amdhsa_uses_dynamic_stack 0
		.amdhsa_enable_private_segment 0
		.amdhsa_system_sgpr_workgroup_id_x 1
		.amdhsa_system_sgpr_workgroup_id_y 0
		.amdhsa_system_sgpr_workgroup_id_z 0
		.amdhsa_system_sgpr_workgroup_info 0
		.amdhsa_system_vgpr_workitem_id 0
		.amdhsa_next_free_vgpr 251
		.amdhsa_next_free_sgpr 102
		.amdhsa_accum_offset 252
		.amdhsa_reserve_vcc 1
		.amdhsa_float_round_mode_32 0
		.amdhsa_float_round_mode_16_64 0
		.amdhsa_float_denorm_mode_32 3
		.amdhsa_float_denorm_mode_16_64 3
		.amdhsa_dx10_clamp 1
		.amdhsa_ieee_mode 1
		.amdhsa_fp16_overflow 0
		.amdhsa_tg_split 0
		.amdhsa_exception_fp_ieee_invalid_op 0
		.amdhsa_exception_fp_denorm_src 0
		.amdhsa_exception_fp_ieee_div_zero 0
		.amdhsa_exception_fp_ieee_overflow 0
		.amdhsa_exception_fp_ieee_underflow 0
		.amdhsa_exception_fp_ieee_inexact 0
		.amdhsa_exception_int_div_zero 0
	.end_amdhsa_kernel

; __global__ void __launch_bounds__(NWAVES * 64, 2) fwd_kernel(Args args) {
;     extern __shared__ __attribute__((aligned(16))) unsigned char lds[];
;     Frame F;
;     F.lds = lds; F.tid = threadIdx.x; F.lane = F.tid & 63; F.wave = __builtin_amdgcn_readfirstlane(F.tid >> 6);
amdhsa.kernels:
  - .agpr_count:     0
    .args:
      - .offset:         0
        .size:           208
        .value_kind:     by_value
      - .offset:         208
        .size:           4
        .value_kind:     hidden_block_count_x
      - .offset:         212
        .size:           4
        .value_kind:     hidden_block_count_y
      - .offset:         216
        .size:           4
        .value_kind:     hidden_block_count_z
      - .offset:         220
        .size:           2
        .value_kind:     hidden_group_size_x
      - .offset:         222
        .size:           2
        .value_kind:     hidden_group_size_y
      - .offset:         224
        .size:           2
        .value_kind:     hidden_group_size_z
      - .offset:         226
        .size:           2
        .value_kind:     hidden_remainder_x
      - .offset:         228
        .size:           2
        .value_kind:     hidden_remainder_y
      - .offset:         230
        .size:           2
        .value_kind:     hidden_remainder_z
      - .offset:         248
        .size:           8
        .value_kind:     hidden_global_offset_x
      - .offset:         256
        .size:           8
        .value_kind:     hidden_global_offset_y
      - .offset:         264
        .size:           8
        .value_kind:     hidden_global_offset_z
      - .offset:         272
        .size:           2
        .value_kind:     hidden_grid_dims
      - .offset:         328
        .size:           4
        .value_kind:     hidden_dynamic_lds_size
    .group_segment_fixed_size: 0
    .kernarg_segment_align: 8
    .kernarg_segment_size: 464
    .language:       OpenCL C
    .language_version:
      - 2
      - 0
    .max_flat_workgroup_size: 512
    .name:           _Z10fwd_kernel4Args
    .private_segment_fixed_size: 0
    .sgpr_count:     108
    .sgpr_spill_count: 4
    .symbol:         _Z10fwd_kernel4Args.kd
    .uniform_work_group_size: 1
    .uses_dynamic_stack: false
    .vgpr_count:     251
    .vgpr_spill_count: 0
    .wavefront_size: 64
